# GEMM3 routing tail: the 28 dependent expert-scale gathers of a row are issued up front instead of in 8 serialized load/wait/store rounds
# baseline (speedup 1.0000x reference)
; #define PG8_LAS __attribute__((address_space(3)))
; #define RT_BAR() do { asm volatile("s_waitcnt lgkmcnt(0)" ::: "memory"); __builtin_amdgcn_s_barrier(); asm volatile("" ::: "memory"); } while (0)
;     __device__ __forceinline__ void fused(f32x4 (&acc)[2][2][4][2], const Unit& u, int wr, int wc, int fr, int fq, PG8_LAS unsigned char* lds, int wid, int lane) const {
;     ...
;             RT_BAR();
;         }
;         if (half == 0) {
;             PG8_LAS int* idxl = (PG8_LAS int*)(lds + 65536) + row * 32;
;             float v0[16], v1[16];
; #pragma unroll
;             for (int q = 0; q < 16; ++q) { const unsigned b0 = __float_as_uint(top0[q]), b1 = __float_as_uint(top1[q]);
;                 v0[q] = __uint_as_float(b0 & ~127u); v1[q] = __uint_as_float(b1 & ~127u); idxl[q] = (int)(b0 & 127u); idxl[16 + q] = (int)(b1 & 127u); }
;             float best[16];
;             { float cv[16]; cv[0] = __uint_as_float((__float_as_uint(v0[0] + v1[0]) & ~255u) | 0u); cv[1] = __uint_as_float((__float_as_uint(v0[0] + v1[1]) & ~255u) | 1u); cv[2] = __uint_as_float((__float_as_uint(v0[0] + v1[2]) & ~255u) | 2u); cv[3] = __uint_as_float((__float_as_uint(v0[0] + v1[3]) & ~255u) | 3u); cv[4] = __uint_as_float((__float_as_uint(v0[0] + v1[4]) & ~255u) | 4u); cv[5] = __uint_as_float((__float_as_uint(v0[0] + v1[5]) & ~255u) | 5u); cv[6] = __uint_as_float((__float_as_uint(v0[0] + v1[6]) & ~255u) | 6u); cv[7] = __uint_as_float((__float_as_uint(v0[0] + v1[7]) & ~255u) | 7u); cv[8] = __uint_as_float((__float_as_uint(v0[0] + v1[8]) & ~255u) | 8u); cv[9] = __uint_as_float((__float_as_uint(v0[0] + v1[9]) & ~255u) | 9u); cv[10] = __uint_as_float((__float_as_uint(v0[0] + v1[10]) & ~255u) | 10u); cv[11] = __uint_as_float((__float_as_uint(v0[0] + v1[11]) & ~255u) | 11u); cv[12] = __uint_as_float((__float_as_uint(v0[0] + v1[12]) & ~255u) | 12u); cv[13] = __uint_as_float((__float_as_uint(v0[0] + v1[13]) & ~255u) | 13u); cv[14] = __uint_as_float((__float_as_uint(v0[0] + v1[14]) & ~255u) | 14u); cv[15] = __uint_as_float((__float_as_uint(v0[0] + v1[15]) & ~255u) | 15u); sort16_desc(cv);
; #pragma unroll
;               for (int q = 0; q < 16; ++q) best[q] = cv[q]; }
.LBB0_588:
	s_waitcnt lgkmcnt(0)
	s_barrier
	s_and_b64 vcc, exec, s[4:5]
	s_cbranch_vccnz .LBB0_590
	v_lshl_add_u32 v16, v128, 7, 0
	v_add_u32_e32 v16, 0x10000, v16
	v_and_b32_e32 v17, 0xffffff80, v12
	v_and_b32_e32 v18, 0xffffff80, v13
	v_and_b32_e32 v21, 0x7f, v77
	v_and_b32_e32 v20, 0x7f, v76
	v_and_b32_e32 v13, 0x7f, v13
	v_and_b32_e32 v12, 0x7f, v12
	v_and_b32_e32 v26, 0xffffff80, v14
	v_and_b32_e32 v28, 0xffffff80, v15
	v_and_b32_e32 v23, 0x7f, v79
	v_and_b32_e32 v22, 0x7f, v78
	v_and_b32_e32 v15, 0x7f, v15
	v_and_b32_e32 v14, 0x7f, v14
	ds_write_b128 v16, v[20:23]
	ds_write_b128 v16, v[12:15] offset:64
	v_and_b32_e32 v21, 0xffffff80, v8
	v_and_b32_e32 v23, 0xffffff80, v9
	v_and_b32_e32 v13, 0x7f, v73
	v_and_b32_e32 v12, 0x7f, v72
	v_and_b32_e32 v9, 0x7f, v9
	v_and_b32_e32 v8, 0x7f, v8
	v_and_b32_e32 v30, 0xffffff80, v10
	v_and_b32_e32 v32, 0xffffff80, v11
	v_and_b32_e32 v15, 0x7f, v75
	v_and_b32_e32 v14, 0x7f, v74
	v_and_b32_e32 v11, 0x7f, v11
	v_and_b32_e32 v10, 0x7f, v10
	v_and_b32_e32 v19, 0xffffff80, v76
	ds_write_b128 v16, v[12:15] offset:16
	ds_write_b128 v16, v[8:11] offset:80
	v_and_b32_e32 v13, 0xffffff80, v4
	v_and_b32_e32 v15, 0xffffff80, v5
	v_and_b32_e32 v9, 0x7f, v69
	v_and_b32_e32 v8, 0x7f, v68
	v_and_b32_e32 v5, 0x7f, v5
	v_and_b32_e32 v4, 0x7f, v4
	v_and_b32_e32 v34, 0xffffff80, v6
	v_and_b32_e32 v36, 0xffffff80, v7
	v_and_b32_e32 v11, 0x7f, v71
	v_and_b32_e32 v10, 0x7f, v70
	v_and_b32_e32 v7, 0x7f, v7
	v_and_b32_e32 v6, 0x7f, v6
	ds_write_b128 v16, v[8:11] offset:32
	ds_write_b128 v16, v[4:7] offset:96
	v_and_b32_e32 v5, 0x7f, v65
	v_and_b32_e32 v4, 0x7f, v64
	v_and_b32_e32 v41, 0xffffff80, v2
	v_and_b32_e32 v42, 0xffffff80, v3
	v_and_b32_e32 v7, 0x7f, v67
	v_and_b32_e32 v6, 0x7f, v66
	v_and_b32_e32 v11, 0x7f, v3
	v_and_b32_e32 v10, 0x7f, v2
	v_add_f32_e32 v2, v19, v17
	s_movk_i32 s4, 0xff00
	v_add_f32_e32 v3, v19, v18
	v_and_b32_e32 v24, 0xffffff80, v77
	ds_write_b128 v16, v[4:7] offset:48
	v_and_b32_e32 v2, 0xffffff00, v2
	v_and_or_b32 v3, v3, s4, 1
	v_add_f32_e32 v4, v19, v26
	v_add_f32_e32 v5, v19, v28
	v_and_b32_e32 v40, 0xffffff80, v1
	v_and_b32_e32 v9, 0x7f, v1
	v_and_b32_e32 v8, 0x7f, v0
	v_and_or_b32 v4, v4, s4, 2
	v_and_or_b32 v5, v5, s4, 3
	v_add_f32_e32 v48, v24, v17
	v_add_f32_e32 v49, v24, v18
	ds_write_b128 v16, v[8:11] offset:112
	v_add_f32_e32 v6, v19, v21
	v_add_f32_e32 v7, v19, v23
	v_add_f32_e32 v11, v19, v15
	v_add_f32_e32 v15, v19, v36
	v_add_f32_e32 v36, v19, v40
	v_max_f32_e32 v40, v2, v3
	v_min_f32_e32 v2, v2, v3
	v_max_f32_e32 v3, v5, v5
	v_and_or_b32 v48, v48, s4, 16
	v_and_or_b32 v49, v49, s4, 17
	v_add_f32_e32 v50, v24, v26
	v_add_f32_e32 v51, v24, v28
	v_and_or_b32 v6, v6, s4, 4
	v_and_or_b32 v7, v7, s4, 5
	v_add_f32_e32 v8, v19, v30
	v_add_f32_e32 v9, v19, v32
	v_max_f32_e32 v5, v4, v3
	v_min_f32_e32 v3, v4, v3
	v_and_or_b32 v50, v50, s4, 18
	v_and_or_b32 v51, v51, s4, 19
	v_and_or_b32 v8, v8, s4, 6
	v_and_or_b32 v9, v9, s4, 7
	v_max_f32_e32 v4, v40, v5
	v_min_f32_e32 v5, v40, v5
	v_max_f32_e32 v40, v2, v3
	v_add_f32_e32 v52, v24, v21
	v_add_f32_e32 v23, v24, v23
	v_add_f32_e32 v30, v24, v30
	v_add_f32_e32 v24, v24, v32
	v_max_f32_e32 v58, v48, v49
	v_min_f32_e32 v48, v48, v49
	v_max_f32_e32 v49, v51, v51
	v_min_f32_e32 v2, v2, v3
	v_max_f32_e32 v3, v40, v5
	v_min_f32_e32 v5, v40, v5
	v_max_f32_e32 v40, v6, v7
	v_min_f32_e32 v6, v6, v7
	v_max_f32_e32 v7, v9, v9
	v_and_or_b32 v52, v52, s4, 20
	v_and_or_b32 v23, v23, s4, 21
	v_and_or_b32 v30, v30, s4, 22
	v_and_or_b32 v24, v24, s4, 23
	v_max_f32_e32 v51, v50, v49
	v_min_f32_e32 v49, v50, v49
	v_max_f32_e32 v9, v8, v7
	v_min_f32_e32 v7, v8, v7
	v_max_f32_e32 v50, v58, v51
	v_min_f32_e32 v51, v58, v51
	v_max_f32_e32 v58, v48, v49
	v_max_f32_e32 v8, v40, v9
	v_min_f32_e32 v9, v40, v9
	v_max_f32_e32 v40, v6, v7
	v_min_f32_e32 v48, v48, v49
	v_max_f32_e32 v49, v58, v51
	v_min_f32_e32 v51, v58, v51
	v_max_f32_e32 v58, v52, v23
	v_min_f32_e32 v23, v52, v23
	v_max_f32_e32 v52, v30, v24
	v_min_f32_e32 v24, v30, v24
	v_min_f32_e32 v6, v6, v7
	v_max_f32_e32 v7, v40, v9
	v_min_f32_e32 v9, v40, v9
	v_max_f32_e32 v30, v58, v52
	v_min_f32_e32 v52, v58, v52
	v_max_f32_e32 v58, v23, v24
	v_max_f32_e32 v40, v4, v8
	v_min_f32_e32 v4, v4, v8
	v_max_f32_e32 v8, v5, v9
	v_min_f32_e32 v23, v23, v24
	v_max_f32_e32 v24, v58, v52
	v_min_f32_e32 v52, v58, v52
	v_and_b32_e32 v25, 0xffffff80, v78
	v_add_f32_e32 v10, v19, v13
	v_min_f32_e32 v5, v5, v9
	v_max_f32_e32 v9, v8, v4
	v_min_f32_e32 v4, v8, v4
	v_max_f32_e32 v8, v3, v7
	v_min_f32_e32 v3, v3, v7
	v_max_f32_e32 v7, v2, v6
	v_max_f32_e32 v58, v50, v30
	v_min_f32_e32 v30, v50, v30
	v_max_f32_e32 v50, v51, v52
	v_and_or_b32 v10, v10, s4, 8
	v_and_or_b32 v11, v11, s4, 9
	v_add_f32_e32 v13, v19, v34
	v_min_f32_e32 v2, v2, v6
	v_max_f32_e32 v6, v7, v3
	v_min_f32_e32 v3, v7, v3
	v_add_f32_e32 v32, v25, v17
	v_add_f32_e32 v53, v25, v18
	v_min_f32_e32 v51, v51, v52
	v_max_f32_e32 v52, v50, v30
	v_min_f32_e32 v30, v50, v30
	v_max_f32_e32 v50, v49, v24
	v_min_f32_e32 v24, v49, v24
	v_max_f32_e32 v49, v48, v23
	v_and_or_b32 v13, v13, s4, 10
	v_and_or_b32 v15, v15, s4, 11
	v_max_f32_e32 v7, v8, v9
	v_min_f32_e32 v8, v8, v9
	v_max_f32_e32 v9, v6, v4
	v_min_f32_e32 v4, v6, v4
	v_max_f32_e32 v6, v3, v5
	v_min_f32_e32 v3, v3, v5
	v_max_f32_e32 v5, v11, v11
	v_and_or_b32 v32, v32, s4, 32
	v_and_or_b32 v53, v53, s4, 33
	v_add_f32_e32 v54, v25, v26
	v_add_f32_e32 v55, v25, v28
	v_min_f32_e32 v23, v48, v23
	v_max_f32_e32 v48, v49, v24
	v_min_f32_e32 v24, v49, v24
	v_and_b32_e32 v27, 0xffffff80, v79
	v_and_b32_e32 v38, 0xffffff80, v0
	v_max_f32_e32 v11, v10, v5
	v_min_f32_e32 v5, v10, v5
	v_max_f32_e32 v10, v15, v15
;     __device__ __forceinline__ void fused(f32x4 (&acc)[2][2][4][2], const Unit& u, int wr, int wc, int fr, int fq, PG8_LAS unsigned char* lds, int wid, int lane) const {
;     ...
;             { float cv[16]; cv[0] = __uint_as_float((__float_as_uint(v0[0] + v1[0]) & ~255u) | 0u); cv[1] = __uint_as_float((__float_as_uint(v0[0] + v1[1]) & ~255u) | 1u); cv[2] = __uint_as_float((__float_as_uint(v0[0] + v1[2]) & ~255u) | 2u); cv[3] = __uint_as_float((__float_as_uint(v0[0] + v1[3]) & ~255u) | 3u); cv[4] = __uint_as_float((__float_as_uint(v0[0] + v1[4]) & ~255u) | 4u); cv[5] = __uint_as_float((__float_as_uint(v0[0] + v1[5]) & ~255u) | 5u); cv[6] = __uint_as_float((__float_as_uint(v0[0] + v1[6]) & ~255u) | 6u); cv[7] = __uint_as_float((__float_as_uint(v0[0] + v1[7]) & ~255u) | 7u); cv[8] = __uint_as_float((__float_as_uint(v0[0] + v1[8]) & ~255u) | 8u); cv[9] = __uint_as_float((__float_as_uint(v0[0] + v1[9]) & ~255u) | 9u); cv[10] = __uint_as_float((__float_as_uint(v0[0] + v1[10]) & ~255u) | 10u); cv[11] = __uint_as_float((__float_as_uint(v0[0] + v1[11]) & ~255u) | 11u); cv[12] = __uint_as_float((__float_as_uint(v0[0] + v1[12]) & ~255u) | 12u); cv[13] = __uint_as_float((__float_as_uint(v0[0] + v1[13]) & ~255u) | 13u); cv[14] = __uint_as_float((__float_as_uint(v0[0] + v1[14]) & ~255u) | 14u); cv[15] = __uint_as_float((__float_as_uint(v0[0] + v1[15]) & ~255u) | 15u); sort16_desc(cv);
; #pragma unroll
;               for (int q = 0; q < 16; ++q) best[q] = cv[q]; }
	v_and_or_b32 v54, v54, s4, 34
	v_and_or_b32 v55, v55, s4, 35
	v_max_f32_e32 v49, v50, v52
	v_min_f32_e32 v50, v50, v52
	v_max_f32_e32 v52, v48, v30
	v_min_f32_e32 v30, v48, v30
	v_max_f32_e32 v48, v24, v51
	v_min_f32_e32 v24, v24, v51
	v_max_f32_e32 v51, v53, v53
	v_add_f32_e32 v34, v19, v38
	v_max_f32_e32 v15, v13, v10
	v_min_f32_e32 v10, v13, v10
	v_add_f32_e32 v21, v25, v21
	v_add_f32_e32 v25, v27, v17
	v_max_f32_e32 v53, v32, v51
	v_min_f32_e32 v32, v32, v51
	v_max_f32_e32 v51, v55, v55
	v_and_or_b32 v34, v34, s4, 12
	v_and_or_b32 v36, v36, s4, 13
	v_add_f32_e32 v38, v19, v41
	v_add_f32_e32 v19, v19, v42
	v_max_f32_e32 v13, v11, v15
	v_min_f32_e32 v11, v11, v15
	v_max_f32_e32 v15, v5, v10
	v_and_or_b32 v21, v21, s4, 36
	v_and_or_b32 v25, v25, s4, 48
	v_add_f32_e32 v56, v27, v18
	v_add_f32_e32 v57, v27, v26
	v_max_f32_e32 v55, v54, v51
	v_min_f32_e32 v51, v54, v51
	v_and_or_b32 v38, v38, s4, 14
	v_and_or_b32 v19, v19, s4, 15
	v_min_f32_e32 v5, v5, v10
	v_max_f32_e32 v10, v15, v11
	v_min_f32_e32 v11, v15, v11
	v_max_f32_e32 v15, v36, v36
	v_and_or_b32 v56, v56, s4, 49
	v_and_or_b32 v57, v57, s4, 50
	v_max_f32_e32 v54, v53, v55
	v_min_f32_e32 v53, v53, v55
	v_max_f32_e32 v55, v32, v51
	v_max_f32_e32 v36, v34, v15
	v_min_f32_e32 v15, v34, v15
	v_max_f32_e32 v34, v38, v38
	v_min_f32_e32 v32, v32, v51
	v_max_f32_e32 v51, v55, v53
	v_min_f32_e32 v53, v55, v53
	v_max_f32_e32 v55, v21, v25
	v_min_f32_e32 v21, v21, v25
	v_max_f32_e32 v25, v57, v57
	v_max_f32_e32 v38, v34, v19
	v_min_f32_e32 v19, v34, v19
	v_max_f32_e32 v57, v56, v25
	v_min_f32_e32 v25, v56, v25
	v_max_f32_e32 v34, v36, v38
	v_min_f32_e32 v36, v36, v38
	v_max_f32_e32 v38, v15, v19
	v_max_f32_e32 v56, v55, v57
	v_min_f32_e32 v55, v55, v57
	v_max_f32_e32 v57, v21, v25
	v_min_f32_e32 v15, v15, v19
	v_max_f32_e32 v19, v38, v36
	v_min_f32_e32 v36, v38, v36
	v_min_f32_e32 v21, v21, v25
	v_max_f32_e32 v25, v57, v55
	v_min_f32_e32 v55, v57, v55
	v_max_f32_e32 v38, v13, v34
	v_min_f32_e32 v13, v13, v34
	v_max_f32_e32 v34, v11, v36
	v_max_f32_e32 v57, v54, v56
	v_min_f32_e32 v54, v54, v56
	v_max_f32_e32 v56, v53, v55
	v_min_f32_e32 v11, v11, v36
	v_max_f32_e32 v36, v34, v13
	v_min_f32_e32 v13, v34, v13
	v_max_f32_e32 v34, v10, v19
	v_min_f32_e32 v10, v10, v19
	v_max_f32_e32 v19, v5, v15
	v_min_f32_e32 v53, v53, v55
	v_max_f32_e32 v55, v56, v54
	v_min_f32_e32 v54, v56, v54
	v_max_f32_e32 v56, v51, v25
	v_min_f32_e32 v25, v51, v25
	v_max_f32_e32 v51, v32, v21
	v_min_f32_e32 v5, v5, v15
	v_max_f32_e32 v15, v19, v10
	v_min_f32_e32 v21, v32, v21
	v_max_f32_e32 v32, v51, v25
	v_min_f32_e32 v10, v19, v10
	v_max_f32_e32 v19, v34, v36
	v_min_f32_e32 v34, v34, v36
	v_max_f32_e32 v36, v15, v13
	v_min_f32_e32 v13, v15, v13
	v_min_f32_e32 v25, v51, v25
	v_max_f32_e32 v51, v56, v55
	v_min_f32_e32 v55, v56, v55
	v_max_f32_e32 v56, v32, v54
	v_min_f32_e32 v32, v32, v54
	v_max_f32_e32 v15, v10, v11
	v_min_f32_e32 v10, v10, v11
	v_min_f32_e32 v11, v40, v38
	v_max_f32_e32 v41, v4, v13
	v_max_f32_e32 v54, v25, v53
	v_min_f32_e32 v25, v25, v53
	v_min_f32_e32 v53, v58, v57
	v_max_f32_e32 v59, v30, v32
	v_min_f32_e32 v4, v4, v13
	v_max_f32_e32 v13, v41, v11
	v_min_f32_e32 v11, v41, v11
	v_max_f32_e32 v41, v8, v34
	v_min_f32_e32 v8, v8, v34
	v_max_f32_e32 v34, v3, v10
	v_min_f32_e32 v30, v30, v32
	v_max_f32_e32 v32, v59, v53
	v_min_f32_e32 v53, v59, v53
	v_max_f32_e32 v59, v50, v55
	v_min_f32_e32 v50, v50, v55
	v_max_f32_e32 v55, v24, v25
	v_min_f32_e32 v3, v3, v10
	v_max_f32_e32 v10, v34, v8
	v_min_f32_e32 v8, v34, v8
	v_min_f32_e32 v24, v24, v25
	v_max_f32_e32 v25, v55, v50
	v_min_f32_e32 v50, v55, v50
	v_max_f32_e32 v34, v41, v13
	v_min_f32_e32 v13, v41, v13
	v_max_f32_e32 v41, v10, v11
	v_min_f32_e32 v10, v10, v11
	v_max_f32_e32 v11, v8, v4
	v_min_f32_e32 v4, v8, v4
	v_max_f32_e32 v8, v7, v19
	v_min_f32_e32 v7, v7, v19
	v_max_f32_e32 v19, v6, v15
	v_max_f32_e32 v55, v59, v32
	v_min_f32_e32 v32, v59, v32
	v_max_f32_e32 v59, v25, v53
	v_min_f32_e32 v25, v25, v53
	v_max_f32_e32 v53, v50, v30
	v_min_f32_e32 v30, v50, v30
	v_max_f32_e32 v50, v49, v51
	v_min_f32_e32 v49, v49, v51
	v_max_f32_e32 v51, v48, v54
	v_min_f32_e32 v6, v6, v15
	v_max_f32_e32 v15, v19, v7
	v_min_f32_e32 v7, v19, v7
	v_max_f32_e32 v19, v9, v36
	v_min_f32_e32 v9, v9, v36
	v_max_f32_e32 v36, v2, v5
	v_min_f32_e32 v48, v48, v54
	v_max_f32_e32 v54, v51, v49
	v_min_f32_e32 v49, v51, v49
	v_max_f32_e32 v51, v52, v56
	v_min_f32_e32 v52, v52, v56
	v_max_f32_e32 v56, v23, v21
	v_min_f32_e32 v2, v2, v5
	v_max_f32_e32 v5, v36, v9
	v_min_f32_e32 v9, v36, v9
	v_max_f32_e32 v36, v19, v15
	v_min_f32_e32 v21, v23, v21
	v_max_f32_e32 v23, v56, v52
	v_min_f32_e32 v52, v56, v52
	v_and_b32_e32 v20, 0xffffff80, v72
	v_min_f32_e32 v15, v19, v15
	v_max_f32_e32 v19, v5, v7
	v_min_f32_e32 v5, v5, v7
	v_max_f32_e32 v7, v9, v6
	v_min_f32_e32 v6, v9, v6
	v_min_f32_e32 v9, v8, v34
	v_min_f32_e32 v42, v36, v13
	v_max_f32_e32 v56, v51, v54
	v_min_f32_e32 v51, v51, v54
	v_max_f32_e32 v54, v23, v49
	v_min_f32_e32 v23, v23, v49
	v_max_f32_e32 v49, v52, v48
	v_min_f32_e32 v48, v52, v48
	v_and_b32_e32 v39, 0xffffff80, v65
	v_min_f32_e32 v65, v48, v24
	v_max3_f32 v9, v9, v48, v24
	v_max3_f32 v24, v42, v49, v30
	v_add_f32_e32 v27, v27, v28
	v_add_f32_e32 v28, v20, v17
	v_add_f32_e32 v42, v20, v18
	v_add_f32_e32 v20, v20, v26
	v_and_b32_e32 v22, 0xffffff80, v73
	v_and_or_b32 v27, v27, s4, 51
	v_and_or_b32 v28, v28, s4, 64
	v_and_b32_e32 v42, 0xffffff00, v42
	v_and_b32_e32 v20, 0xffffff00, v20
	v_and_b32_e32 v29, 0xffffff80, v74
	v_and_b32_e32 v31, 0xffffff80, v75
	v_and_b32_e32 v33, 0xffffff80, v70
	v_and_b32_e32 v35, 0xffffff80, v71
	v_and_b32_e32 v37, 0xffffff80, v64
;     __device__ __forceinline__ void fused(f32x4 (&acc)[2][2][4][2], const Unit& u, int wr, int wc, int fr, int fq, PG8_LAS unsigned char* lds, int wid, int lane) const {
;     ...
;             { float cv[16]; cv[0] = __uint_as_float((__float_as_uint(v0[1] + v1[0]) & ~255u) | 16u); cv[1] = __uint_as_float((__float_as_uint(v0[1] + v1[1]) & ~255u) | 17u); cv[2] = __uint_as_float((__float_as_uint(v0[1] + v1[2]) & ~255u) | 18u); cv[3] = __uint_as_float((__float_as_uint(v0[1] + v1[3]) & ~255u) | 19u); cv[4] = __uint_as_float((__float_as_uint(v0[1] + v1[4]) & ~255u) | 20u); cv[5] = __uint_as_float((__float_as_uint(v0[1] + v1[5]) & ~255u) | 21u); cv[6] = __uint_as_float((__float_as_uint(v0[1] + v1[6]) & ~255u) | 22u); cv[7] = __uint_as_float((__float_as_uint(v0[1] + v1[7]) & ~255u) | 23u); cv[8] = __uint_as_float((__float_as_uint(v0[2] + v1[0]) & ~255u) | 32u); cv[9] = __uint_as_float((__float_as_uint(v0[2] + v1[1]) & ~255u) | 33u); cv[10] = __uint_as_float((__float_as_uint(v0[2] + v1[2]) & ~255u) | 34u); cv[11] = __uint_as_float((__float_as_uint(v0[2] + v1[3]) & ~255u) | 35u); cv[12] = __uint_as_float((__float_as_uint(v0[2] + v1[4]) & ~255u) | 36u); cv[13] = __uint_as_float((__float_as_uint(v0[3] + v1[0]) & ~255u) | 48u); cv[14] = __uint_as_float((__float_as_uint(v0[3] + v1[1]) & ~255u) | 49u); cv[15] = __uint_as_float((__float_as_uint(v0[3] + v1[2]) & ~255u) | 50u); sort16_desc(cv); merge_top16(best, cv); }
	v_min_f32_e32 v43, v15, v41
	v_min_f32_e32 v44, v19, v10
	v_min_f32_e32 v62, v54, v25
	v_or_b32_e32 v42, 0x41, v42
	v_or_b32_e32 v20, 0x42, v20
	v_add_f32_e32 v26, v22, v17
	v_add_f32_e32 v22, v22, v18
	v_min_f32_e32 v63, v23, v53
	v_max3_f32 v23, v43, v23, v53
	v_max3_f32 v10, v19, v10, v62
	v_max3_f32 v19, v44, v54, v25
	v_and_b32_e32 v26, 0xffffff00, v26
	v_and_b32_e32 v22, 0xffffff00, v22
	v_add_f32_e32 v43, v29, v17
	v_add_f32_e32 v29, v29, v18
	v_add_f32_e32 v44, v31, v17
	v_add_f32_e32 v18, v31, v18
	v_add_f32_e32 v31, v33, v17
	v_add_f32_e32 v33, v35, v17
	v_add_f32_e32 v35, v37, v17
	v_add_f32_e32 v37, v39, v17
	v_max_f32_e32 v39, v27, v28
	v_min_f32_e32 v27, v27, v28
	v_max_f32_e32 v28, v42, v42
	v_or_b32_e32 v26, 0x50, v26
	v_or_b32_e32 v22, 0x51, v22
	v_and_b32_e32 v43, 0xffffff00, v43
	v_and_b32_e32 v29, 0xffffff00, v29
	v_max_f32_e32 v42, v28, v20
	v_min_f32_e32 v20, v28, v20
	v_or_b32_e32 v43, 0x60, v43
	v_or_b32_e32 v29, 0x61, v29
	v_max_f32_e32 v28, v39, v42
	v_min_f32_e32 v39, v39, v42
	v_max_f32_e32 v42, v27, v20
	v_min_f32_e32 v20, v27, v20
	v_max_f32_e32 v27, v42, v39
	v_min_f32_e32 v39, v42, v39
	v_max_f32_e32 v42, v26, v22
	v_min_f32_e32 v22, v26, v22
	v_max_f32_e32 v26, v29, v29
	v_max_f32_e32 v29, v43, v43
	v_max_f32_e32 v43, v29, v26
	v_min_f32_e32 v26, v29, v26
	v_max_f32_e32 v29, v42, v43
	v_min_f32_e32 v42, v42, v43
	v_max_f32_e32 v43, v22, v26
	v_and_b32_e32 v12, 0xffffff80, v68
	v_and_b32_e32 v14, 0xffffff80, v69
	v_min_f32_e32 v22, v22, v26
	v_max_f32_e32 v26, v43, v42
	v_min_f32_e32 v42, v43, v42
	v_add_f32_e32 v12, v12, v17
	v_add_f32_e32 v14, v14, v17
	v_max_f32_e32 v43, v28, v29
	v_min_f32_e32 v28, v28, v29
	v_max_f32_e32 v29, v39, v42
	v_and_b32_e32 v44, 0xffffff00, v44
	v_and_b32_e32 v18, 0xffffff00, v18
	v_and_b32_e32 v12, 0xffffff00, v12
	v_and_b32_e32 v14, 0xffffff00, v14
	v_min_f32_e32 v39, v39, v42
	v_max_f32_e32 v42, v29, v28
	v_min_f32_e32 v28, v29, v28
	v_max_f32_e32 v29, v27, v26
	v_min_f32_e32 v26, v27, v26
	v_max_f32_e32 v27, v20, v22
	v_or_b32_e32 v44, 0x70, v44
	v_or_b32_e32 v18, 0x71, v18
	v_or_b32_e32 v12, 0x80, v12
	v_or_b32_e32 v14, 0x90, v14
	v_min_f32_e32 v20, v20, v22
	v_max_f32_e32 v22, v27, v26
	v_min_f32_e32 v26, v27, v26
	v_and_b32_e32 v31, 0xffffff00, v31
	v_and_b32_e32 v33, 0xffffff00, v33
	v_max_f32_e32 v27, v29, v42
	v_min_f32_e32 v29, v29, v42
	v_max_f32_e32 v42, v22, v28
	v_min_f32_e32 v22, v22, v28
	v_max_f32_e32 v28, v26, v39
	v_min_f32_e32 v26, v26, v39
	v_max_f32_e32 v39, v44, v44
	v_or_b32_e32 v31, 0xa0, v31
	v_or_b32_e32 v33, 0xb0, v33
	v_and_b32_e32 v35, 0xffffff00, v35
	v_and_b32_e32 v37, 0xffffff00, v37
	v_max_f32_e32 v44, v39, v18
	v_min_f32_e32 v18, v39, v18
	v_max_f32_e32 v39, v12, v14
	v_min_f32_e32 v12, v12, v14
	v_or_b32_e32 v35, 0xc0, v35
	v_or_b32_e32 v37, 0xd0, v37
	v_max_f32_e32 v14, v44, v39
	v_min_f32_e32 v39, v44, v39
	v_max_f32_e32 v44, v18, v12
	v_min_f32_e32 v12, v18, v12
	v_max_f32_e32 v18, v44, v39
	v_min_f32_e32 v39, v44, v39
	v_max_f32_e32 v44, v31, v33
	v_min_f32_e32 v31, v31, v33
	v_max_f32_e32 v33, v37, v37
	v_max_f32_e32 v37, v35, v33
	v_min_f32_e32 v33, v35, v33
	v_max_f32_e32 v35, v44, v37
	v_min_f32_e32 v37, v44, v37
	v_max_f32_e32 v44, v31, v33
	v_min_f32_e32 v31, v31, v33
	v_max_f32_e32 v33, v44, v37
	v_min_f32_e32 v37, v44, v37
	v_max_f32_e32 v44, v14, v35
	v_min_f32_e32 v14, v14, v35
	v_max_f32_e32 v35, v39, v37
	v_min_f32_e32 v37, v39, v37
	v_max_f32_e32 v39, v35, v14
	v_min_f32_e32 v14, v35, v14
	v_max_f32_e32 v35, v18, v33
	v_min_f32_e32 v18, v18, v33
	v_max_f32_e32 v33, v12, v31
	v_min_f32_e32 v12, v12, v31
	v_max_f32_e32 v31, v33, v18
	v_min_f32_e32 v45, v5, v11
	v_min_f32_e32 v61, v51, v59
	v_min_f32_e32 v18, v33, v18
	v_max_f32_e32 v33, v35, v39
	v_min_f32_e32 v35, v35, v39
	v_max_f32_e32 v39, v31, v14
	v_min_f32_e32 v14, v31, v14
	v_max3_f32 v5, v5, v11, v61
	v_max3_f32 v11, v45, v51, v59
	v_max_f32_e32 v31, v18, v37
	v_min_f32_e32 v18, v18, v37
	v_min_f32_e32 v37, v43, v44
	v_max_f32_e32 v45, v22, v14
	v_min_f32_e32 v14, v22, v14
	v_max_f32_e32 v22, v45, v37
	v_min_f32_e32 v37, v45, v37
	v_max_f32_e32 v45, v29, v35
	v_min_f32_e32 v29, v29, v35
	v_max_f32_e32 v35, v26, v18
	v_min_f32_e32 v46, v7, v4
	v_min_f32_e32 v47, v6, v3
	v_min_f32_e32 v52, v50, v55
	v_min_f32_e32 v60, v56, v32
	v_min_f32_e32 v64, v49, v30
	v_min_f32_e32 v18, v26, v18
	v_max_f32_e32 v26, v35, v29
	v_min_f32_e32 v29, v35, v29
	v_max3_f32 v21, v40, v38, v21
	v_max3_f32 v8, v8, v34, v65
	v_max3_f32 v13, v36, v13, v64
	v_max3_f32 v15, v15, v41, v63
	v_max3_f32 v4, v7, v4, v60
	v_max3_f32 v7, v46, v56, v32
	v_max3_f32 v3, v6, v3, v52
	v_max3_f32 v6, v47, v50, v55
	v_max3_f32 v2, v2, v58, v57
	v_max_f32_e32 v35, v45, v22
	v_min_f32_e32 v22, v45, v22
	v_max_f32_e32 v45, v26, v37
	v_min_f32_e32 v26, v26, v37
	v_max_f32_e32 v37, v29, v14
	v_min_f32_e32 v14, v29, v14
	v_max_f32_e32 v29, v27, v33
	v_min_f32_e32 v27, v27, v33
	v_max_f32_e32 v33, v28, v31
	v_max_f32_e32 v25, v21, v19
	v_min_f32_e32 v19, v21, v19
	v_max_f32_e32 v21, v8, v5
	v_min_f32_e32 v5, v8, v5
	v_max_f32_e32 v8, v9, v11
	v_min_f32_e32 v9, v9, v11
	v_max_f32_e32 v11, v13, v4
	v_min_f32_e32 v4, v13, v4
	v_max_f32_e32 v13, v24, v7
	v_min_f32_e32 v7, v24, v7
	v_max_f32_e32 v24, v15, v3
	v_min_f32_e32 v3, v15, v3
	v_max_f32_e32 v15, v23, v6
	v_min_f32_e32 v6, v23, v6
	v_max_f32_e32 v23, v10, v2
	v_min_f32_e32 v2, v10, v2
	v_min_f32_e32 v28, v28, v31
	v_max_f32_e32 v31, v33, v27
	v_min_f32_e32 v27, v33, v27
	v_max_f32_e32 v33, v42, v39
	v_min_f32_e32 v39, v42, v39
	v_max_f32_e32 v42, v20, v12
	v_max_f32_e32 v10, v25, v13
	v_min_f32_e32 v13, v25, v13
	v_max_f32_e32 v25, v21, v24
	v_min_f32_e32 v21, v21, v24
; __device__ __forceinline__ void merge_top16(float (&v)[16], const float (&nw)[16]) {
;     v[0] = fmaxf(v[0], nw[15]); v[1] = fmaxf(v[1], nw[14]); v[2] = fmaxf(v[2], nw[13]); v[3] = fmaxf(v[3], nw[12]); v[4] = fmaxf(v[4], nw[11]); v[5] = fmaxf(v[5], nw[10]); v[6] = fmaxf(v[6], nw[9]); v[7] = fmaxf(v[7], nw[8]); v[8] = fmaxf(v[8], nw[7]); v[9] = fmaxf(v[9], nw[6]); v[10] = fmaxf(v[10], nw[5]); v[11] = fmaxf(v[11], nw[4]); v[12] = fmaxf(v[12], nw[3]); v[13] = fmaxf(v[13], nw[2]); v[14] = fmaxf(v[14], nw[1]); v[15] = fmaxf(v[15], nw[0]);
;     CE(v[0], v[8]); CE(v[1], v[9]); CE(v[2], v[10]); CE(v[3], v[11]);
;     CE(v[4], v[12]); CE(v[5], v[13]); CE(v[6], v[14]); CE(v[7], v[15]);
;     CE(v[0], v[4]); CE(v[1], v[5]); CE(v[2], v[6]); CE(v[3], v[7]);
;     CE(v[8], v[12]); CE(v[9], v[13]); CE(v[10], v[14]); CE(v[11], v[15]);
;     CE(v[0], v[2]); CE(v[1], v[3]); CE(v[4], v[6]); CE(v[5], v[7]);
;     CE(v[8], v[10]); CE(v[9], v[11]); CE(v[12], v[14]); CE(v[13], v[15]);
;     __device__ __forceinline__ void fused(f32x4 (&acc)[2][2][4][2], const Unit& u, int wr, int wc, int fr, int fq, PG8_LAS unsigned char* lds, int wid, int lane) const {
;     ...
;             { float cv[16]; cv[0] = __uint_as_float((__float_as_uint(v0[14] + v1[0]) & ~255u) | 224u); cv[1] = __uint_as_float((__float_as_uint(v0[15] + v1[0]) & ~255u) | 240u); cv[2] = -INFINITY; cv[3] = -INFINITY; cv[4] = -INFINITY; cv[5] = -INFINITY; cv[6] = -INFINITY; cv[7] = -INFINITY; cv[8] = -INFINITY; cv[9] = -INFINITY; cv[10] = -INFINITY; cv[11] = -INFINITY; cv[12] = -INFINITY; cv[13] = -INFINITY; cv[14] = -INFINITY; cv[15] = -INFINITY; sort16_desc(cv); merge_top16(best, cv); }
;             float sc[16], sum = 0.f;
; #pragma unroll
;             for (int q = 0; q < 16; ++q) { sc[q] = __uint_as_float(__float_as_uint(best[q]) & ~255u); }
;             const float smax = sc[0];
; #pragma unroll
;             for (int q = 0; q < 16; ++q) { sc[q] = __builtin_amdgcn_exp2f((sc[q] - smax) * 1.4426950408889634f); }
; #pragma unroll
;             for (int q = 0; q < 16; ++q) sum += sc[q];
;             const float rs = 1.0f / sum;
;             asm volatile("s_waitcnt lgkmcnt(0)" ::: "memory");
;             int ex[16];
; #pragma unroll
;             for (int q = 0; q < 16; ++q) { const unsigned cid = __float_as_uint(best[q]) & 255u; ex[q] = idxl[cid >> 4] * 128 + idxl[16 + (cid & 15u)]; }
	v_max_f32_e32 v24, v8, v15
	v_min_f32_e32 v8, v8, v15
	v_max_f32_e32 v15, v11, v23
	v_min_f32_e32 v11, v11, v23
	v_max_f32_e32 v23, v19, v7
	v_min_f32_e32 v7, v19, v7
	v_max_f32_e32 v19, v5, v3
	v_min_f32_e32 v3, v5, v3
	v_max_f32_e32 v5, v9, v6
	v_min_f32_e32 v6, v9, v6
	v_max_f32_e32 v9, v4, v2
	v_min_f32_e32 v2, v4, v2
	v_min_f32_e32 v12, v20, v12
	v_max_f32_e32 v20, v42, v39
	v_min_f32_e32 v39, v42, v39
	v_and_b32_e32 v1, 0xffffff80, v66
	v_and_b32_e32 v0, 0xffffff80, v67
	v_max_f32_e32 v4, v10, v24
	v_min_f32_e32 v10, v10, v24
	v_max_f32_e32 v24, v25, v15
	v_min_f32_e32 v15, v25, v15
	v_max_f32_e32 v25, v13, v8
	v_min_f32_e32 v8, v13, v8
	v_max_f32_e32 v13, v21, v11
	v_min_f32_e32 v11, v21, v11
	v_max_f32_e32 v21, v23, v5
	v_min_f32_e32 v5, v23, v5
	v_max_f32_e32 v23, v19, v9
	v_min_f32_e32 v9, v19, v9
	v_max_f32_e32 v19, v7, v6
	v_min_f32_e32 v6, v7, v6
	v_max_f32_e32 v7, v3, v2
	v_min_f32_e32 v2, v3, v2
	v_max_f32_e32 v42, v33, v31
	v_min_f32_e32 v31, v33, v31
	v_max_f32_e32 v33, v20, v27
	v_min_f32_e32 v20, v20, v27
	v_max_f32_e32 v27, v39, v28
	v_min_f32_e32 v28, v39, v28
	v_min_f32_e32 v3, v4, v24
	v_min_f32_e32 v30, v10, v15
	v_min_f32_e32 v32, v25, v13
	v_min_f32_e32 v34, v8, v11
	v_min_f32_e32 v36, v21, v23
	v_min_f32_e32 v38, v5, v9
	v_min_f32_e32 v40, v19, v7
	v_min_f32_e32 v41, v6, v2
	v_max_f32_e32 v39, v29, v35
	v_min_f32_e32 v29, v29, v35
	v_max_f32_e32 v35, v42, v22
	v_min_f32_e32 v22, v42, v22
	v_max_f32_e32 v42, v31, v45
	v_min_f32_e32 v31, v31, v45
	v_max_f32_e32 v45, v33, v26
	v_min_f32_e32 v26, v33, v26
	v_max_f32_e32 v33, v20, v37
	v_min_f32_e32 v20, v20, v37
	v_max_f32_e32 v37, v27, v14
	v_min_f32_e32 v14, v27, v14
	v_max_f32_e32 v27, v28, v18
	v_min_f32_e32 v18, v28, v18
	v_add_f32_e32 v1, v1, v17
	v_add_f32_e32 v0, v0, v17
	v_max3_f32 v4, v4, v24, v12
	v_max_f32_e32 v3, v3, v18
	v_max3_f32 v10, v10, v15, v27
	v_max_f32_e32 v12, v30, v14
	v_max3_f32 v13, v25, v13, v37
	v_max_f32_e32 v14, v32, v20
	v_max3_f32 v8, v8, v11, v33
	v_max_f32_e32 v11, v34, v26
	v_max3_f32 v15, v21, v23, v45
	v_max_f32_e32 v18, v36, v31
	v_max3_f32 v5, v5, v9, v42
	v_max_f32_e32 v9, v38, v22
	v_max3_f32 v7, v19, v7, v35
	v_max_f32_e32 v19, v40, v29
	v_max3_f32 v2, v6, v2, v39
	v_max3_f32 v6, v41, v43, v44
	v_and_b32_e32 v1, 0xffffff00, v1
	v_and_b32_e32 v0, 0xffffff00, v0
	v_max_f32_e32 v20, v4, v15
	v_min_f32_e32 v4, v4, v15
	v_max_f32_e32 v15, v3, v18
	v_min_f32_e32 v3, v3, v18
	v_max_f32_e32 v18, v10, v5
	v_min_f32_e32 v5, v10, v5
	v_max_f32_e32 v10, v12, v9
	v_min_f32_e32 v9, v12, v9
	v_max_f32_e32 v12, v13, v7
	v_min_f32_e32 v7, v13, v7
	v_max_f32_e32 v13, v14, v19
	v_min_f32_e32 v14, v14, v19
	v_max_f32_e32 v19, v8, v2
	v_min_f32_e32 v2, v8, v2
	v_max_f32_e32 v8, v11, v6
	v_min_f32_e32 v6, v11, v6
	v_or_b32_e32 v1, 0xe0, v1
	v_or_b32_e32 v0, 0xf0, v0
	v_max_f32_e32 v11, v20, v12
	v_min_f32_e32 v12, v20, v12
	v_max_f32_e32 v20, v15, v13
	v_min_f32_e32 v13, v15, v13
	v_max_f32_e32 v15, v18, v19
	v_min_f32_e32 v18, v18, v19
	v_max_f32_e32 v19, v10, v8
	v_min_f32_e32 v8, v10, v8
	v_max_f32_e32 v10, v4, v7
	v_min_f32_e32 v4, v4, v7
	v_max_f32_e32 v7, v3, v14
	v_min_f32_e32 v3, v3, v14
	v_max_f32_e32 v14, v5, v2
	v_min_f32_e32 v2, v5, v2
	v_max_f32_e32 v5, v9, v6
	v_min_f32_e32 v6, v9, v6
	v_max_f32_e32 v9, v11, v15
	v_min_f32_e32 v11, v11, v15
	v_max_f32_e32 v15, v20, v19
	v_min_f32_e32 v19, v20, v19
	v_max_f32_e32 v20, v12, v18
	v_min_f32_e32 v12, v12, v18
	v_max_f32_e32 v18, v13, v8
	v_min_f32_e32 v8, v13, v8
	v_max_f32_e32 v13, v10, v14
	v_min_f32_e32 v10, v10, v14
	v_max_f32_e32 v14, v7, v5
	v_min_f32_e32 v5, v7, v5
	v_max_f32_e32 v7, v4, v2
	v_min_f32_e32 v2, v4, v2
	v_max_f32_e32 v4, v3, v6
	v_min_f32_e32 v3, v3, v6
	v_max_f32_e32 v17, v1, v0
	v_min_f32_e32 v0, v1, v0
	v_min_f32_e32 v6, v9, v15
	v_min_f32_e32 v21, v11, v19
	v_min_f32_e32 v22, v20, v18
	v_min_f32_e32 v23, v12, v8
	v_min_f32_e32 v24, v13, v14
	v_min_f32_e32 v25, v10, v5
	v_min_f32_e32 v26, v7, v4
	v_min_f32_e32 v27, v2, v3
	s_mov_b32 s4, 0xff800000
	v_max_f32_e32 v0, 0xff800000, v0
	v_max3_f32 v1, v9, v15, s4
	v_max_f32_e32 v6, 0xff800000, v6
	v_max3_f32 v9, v11, v19, s4
	v_max_f32_e32 v11, 0xff800000, v21
	v_max3_f32 v15, v20, v18, s4
	v_max_f32_e32 v18, 0xff800000, v22
	v_max3_f32 v8, v12, v8, s4
	v_max_f32_e32 v12, 0xff800000, v23
	v_max3_f32 v13, v13, v14, s4
	v_max_f32_e32 v14, 0xff800000, v24
	v_max3_f32 v5, v10, v5, s4
	v_max_f32_e32 v10, 0xff800000, v25
	v_max3_f32 v4, v7, v4, s4
	v_max_f32_e32 v7, 0xff800000, v26
	v_max3_f32 v0, v2, v3, v0
	v_max3_f32 v2, v27, v17, s4
	v_max_f32_e32 v3, v1, v13
	v_min_f32_e32 v1, v1, v13
	v_max_f32_e32 v13, v6, v14
	v_min_f32_e32 v6, v6, v14
	v_max_f32_e32 v14, v9, v5
	v_min_f32_e32 v5, v9, v5
	v_max_f32_e32 v9, v11, v10
	v_min_f32_e32 v10, v11, v10
	v_max_f32_e32 v11, v15, v4
	v_min_f32_e32 v4, v15, v4
	v_max_f32_e32 v15, v18, v7
	v_max_f32_e32 v17, v8, v0
	v_min_f32_e32 v0, v8, v0
	v_max_f32_e32 v8, v12, v2
	v_min_f32_e32 v2, v12, v2
	v_max_f32_e32 v12, v3, v11
	v_min_f32_e32 v3, v3, v11
	v_max_f32_e32 v11, v13, v15
	v_min_f32_e32 v13, v13, v15
	v_max_f32_e32 v15, v14, v17
	v_min_f32_e32 v14, v14, v17
	v_max_f32_e32 v17, v9, v8
	v_min_f32_e32 v8, v9, v8
	v_max_f32_e32 v9, v1, v4
	v_min_f32_e32 v24, v1, v4
	v_max_f32_e32 v27, v5, v0
	v_min_f32_e32 v28, v5, v0
	v_max_f32_e32 v29, v10, v2
	v_min_f32_e32 v30, v10, v2
	v_max_f32_e32 v0, v12, v15
	v_min_f32_e32 v1, v12, v15
	v_max_f32_e32 v2, v11, v17
	v_min_f32_e32 v4, v11, v17
	v_min_f32_e32 v7, v18, v7
	v_max_f32_e32 v33, v0, v2
	v_min_f32_e32 v34, v0, v2
	v_min_f32_e32 v36, v1, v4
	v_max_f32_e32 v25, v6, v7
	v_min_f32_e32 v26, v6, v7
	v_max_f32_e32 v35, v1, v4
	v_lshrrev_b32_e32 v0, 2, v33
	v_lshrrev_b32_e32 v2, 2, v34
	v_lshrrev_b32_e32 v6, 2, v36
	v_max_f32_e32 v17, v3, v14
	v_min_f32_e32 v31, v3, v14
	v_and_b32_e32 v0, 60, v0
	v_and_b32_e32 v1, 15, v33
	v_and_b32_e32 v2, 60, v2
	v_and_b32_e32 v3, 15, v34
	v_lshrrev_b32_e32 v4, 2, v35
	v_and_b32_e32 v5, 15, v35
	v_and_b32_e32 v6, 60, v6
	v_and_b32_e32 v7, 15, v36
	s_waitcnt lgkmcnt(0)
; #define RT_PK(q_) (ex[q_] | (int)((__float_as_uint(usc[ex[q_]]) >> 23) << 14))
;     __device__ __forceinline__ void fused(f32x4 (&acc)[2][2][4][2], const Unit& u, int wr, int wc, int fr, int fq, PG8_LAS unsigned char* lds, int wid, int lane) const {
;     ...
;             for (int q = 0; q < 16; ++q) { sc[q] = __uint_as_float(__float_as_uint(best[q]) & ~255u); }
;             const float smax = sc[0];
; #pragma unroll
;             for (int q = 0; q < 16; ++q) { sc[q] = __builtin_amdgcn_exp2f((sc[q] - smax) * 1.4426950408889634f); }
; #pragma unroll
;             for (int q = 0; q < 16; ++q) sum += sc[q];
;             const float rs = 1.0f / sum;
;             asm volatile("s_waitcnt lgkmcnt(0)" ::: "memory");
;             int ex[16];
; #pragma unroll
;             for (int q = 0; q < 16; ++q) { const unsigned cid = __float_as_uint(best[q]) & 255u; ex[q] = idxl[cid >> 4] * 128 + idxl[16 + (cid & 15u)]; }
;             const size_t o = ((size_t)u.pn * 16384 + (size_t)(u.pm * BM + row)) * 16;
;             typedef int i32x4 __attribute__((ext_vector_type(4)));
; #pragma unroll
;             for (int i = 0; i < 4; ++i) {
;     ...
;                 *(i32x4*)(eidx + o + 4 * i) = (i32x4){RT_PK(4 * i), RT_PK(4 * i + 1), RT_PK(4 * i + 2), RT_PK(4 * i + 3)};
;                 *(f32x4*)(egate + o + 4 * i) = (f32x4){sc[4 * i] * rs * vsc[ex[4 * i]], sc[4 * i + 1] * rs * vsc[ex[4 * i + 1]], sc[4 * i + 2] * rs * vsc[ex[4 * i + 2]], sc[4 * i + 3] * rs * vsc[ex[4 * i + 3]]};
	v_add_u32_e32 v0, v16, v0
	v_lshl_add_u32 v1, v1, 2, v16
	v_add_u32_e32 v2, v16, v2
	v_lshl_add_u32 v3, v3, 2, v16
	v_and_b32_e32 v4, 60, v4
	v_lshl_add_u32 v5, v5, 2, v16
	v_add_u32_e32 v6, v16, v6
	v_lshl_add_u32 v7, v7, 2, v16
	v_add_u32_e32 v4, v16, v4
	ds_read_b32 v0, v0
	ds_read_b32 v1, v1 offset:64
	ds_read_b32 v2, v2
	ds_read_b32 v3, v3 offset:64
	ds_read_b32 v10, v4
	ds_read_b32 v5, v5 offset:64
	ds_read_b32 v6, v6
	ds_read_b32 v7, v7 offset:64
	s_waitcnt lgkmcnt(0)
	v_lshl_add_u32 v0, v0, 7, v1
	v_ashrrev_i32_e32 v1, 31, v0
	v_lshl_add_u32 v4, v2, 7, v3
	v_lshlrev_b64 v[14:15], 2, v[0:1]
	v_lshl_add_u32 v10, v10, 7, v5
	v_lshl_add_u32 v12, v6, 7, v7
	v_lshl_add_u64 v[2:3], s[8:9], 0, v[14:15]
	v_ashrrev_i32_e32 v5, 31, v4
	v_max_f32_e32 v32, v13, v8
	v_min_f32_e32 v8, v13, v8
	global_load_dword v1, v[2:3], off
	v_lshlrev_b64 v[18:19], 2, v[4:5]
	v_ashrrev_i32_e32 v11, 31, v10
	v_ashrrev_i32_e32 v13, 31, v12
	v_lshl_add_u64 v[2:3], s[8:9], 0, v[18:19]
	v_lshlrev_b64 v[20:21], 2, v[10:11]
	v_lshlrev_b64 v[22:23], 2, v[12:13]
	v_lshl_add_u64 v[6:7], s[8:9], 0, v[20:21]
	global_load_dword v5, v[2:3], off
	global_load_dword v11, v[6:7], off
	v_lshl_add_u64 v[2:3], s[8:9], 0, v[22:23]
	global_load_dword v13, v[2:3], off
	v_min_f32_e32 v2, v9, v27
	v_min_f32_e32 v6, v25, v29
	v_max_f32_e32 v43, v2, v6
	v_min_f32_e32 v44, v2, v6
	v_and_b32_e32 v2, 0xffffff00, v34
	v_and_b32_e32 v51, 0xffffff00, v33
	v_max_f32_e32 v37, v9, v27
	v_max_f32_e32 v3, v25, v29
	v_sub_f32_e32 v2, v2, v51
	v_min_f32_e32 v9, v24, v28
	v_min_f32_e32 v25, v26, v30
	v_max_f32_e32 v41, v37, v3
	v_min_f32_e32 v42, v37, v3
	v_and_b32_e32 v3, 0xffffff00, v35
	v_mul_f32_e32 v2, 0x3fb8aa3b, v2
	v_max_f32_e32 v47, v9, v25
	v_min_f32_e32 v48, v9, v25
	v_exp_f32_e32 v25, v2
	v_sub_f32_e32 v2, v3, v51
	v_and_b32_e32 v6, 0xffffff00, v36
	v_mul_f32_e32 v2, 0x3fb8aa3b, v2
	v_max_f32_e32 v7, v24, v28
	v_max_f32_e32 v24, v26, v30
	v_max_f32_e32 v38, v17, v32
	v_exp_f32_e32 v26, v2
	v_sub_f32_e32 v2, v6, v51
	v_max_f32_e32 v45, v7, v24
	v_min_f32_e32 v46, v7, v24
	v_and_b32_e32 v7, 0xffffff00, v38
	v_mul_f32_e32 v2, 0x3fb8aa3b, v2
	v_min_f32_e32 v17, v17, v32
	v_exp_f32_e32 v27, v2
	v_sub_f32_e32 v2, v7, v51
	v_max_f32_e32 v39, v31, v8
	v_min_f32_e32 v40, v31, v8
	v_lshl_add_u64 v[168:169], s[6:7], 0, v[14:15]
	global_load_dword v194, v[168:169], off
	v_lshl_add_u64 v[168:169], s[6:7], 0, v[18:19]
	global_load_dword v195, v[168:169], off
	v_lshl_add_u64 v[168:169], s[6:7], 0, v[20:21]
	global_load_dword v196, v[168:169], off
	v_lshl_add_u64 v[168:169], s[6:7], 0, v[22:23]
	global_load_dword v197, v[168:169], off
	v_lshrrev_b32_e32 v140, 2, v38
	v_and_b32_e32 v141, 15, v38
	v_and_b32_e32 v140, 60, v140
	v_lshl_add_u32 v141, v141, 2, v16
	v_add_u32_e32 v140, v16, v140
	ds_read_b32 v140, v140
	ds_read_b32 v141, v141 offset:64
	v_lshrrev_b32_e32 v142, 2, v17
	v_and_b32_e32 v143, 15, v17
	v_and_b32_e32 v142, 60, v142
	v_lshl_add_u32 v143, v143, 2, v16
	v_add_u32_e32 v142, v16, v142
	ds_read_b32 v142, v142
	ds_read_b32 v143, v143 offset:64
	v_lshrrev_b32_e32 v144, 2, v39
	v_and_b32_e32 v145, 15, v39
	v_and_b32_e32 v144, 60, v144
	v_lshl_add_u32 v145, v145, 2, v16
	v_add_u32_e32 v144, v16, v144
	ds_read_b32 v144, v144
	ds_read_b32 v145, v145 offset:64
	v_lshrrev_b32_e32 v146, 2, v40
	v_and_b32_e32 v147, 15, v40
	v_and_b32_e32 v146, 60, v146
	v_lshl_add_u32 v147, v147, 2, v16
	v_add_u32_e32 v146, v16, v146
	ds_read_b32 v146, v146
	ds_read_b32 v147, v147 offset:64
	v_lshrrev_b32_e32 v148, 2, v41
	v_and_b32_e32 v149, 15, v41
	v_and_b32_e32 v148, 60, v148
	v_lshl_add_u32 v149, v149, 2, v16
	v_add_u32_e32 v148, v16, v148
	ds_read_b32 v148, v148
	ds_read_b32 v149, v149 offset:64
	v_lshrrev_b32_e32 v150, 2, v42
	v_and_b32_e32 v151, 15, v42
	v_and_b32_e32 v150, 60, v150
	v_lshl_add_u32 v151, v151, 2, v16
	v_add_u32_e32 v150, v16, v150
	ds_read_b32 v150, v150
	ds_read_b32 v151, v151 offset:64
	v_lshrrev_b32_e32 v152, 2, v43
	v_and_b32_e32 v153, 15, v43
	v_and_b32_e32 v152, 60, v152
	v_lshl_add_u32 v153, v153, 2, v16
	v_add_u32_e32 v152, v16, v152
	ds_read_b32 v152, v152
	ds_read_b32 v153, v153 offset:64
	v_lshrrev_b32_e32 v154, 2, v44
	v_and_b32_e32 v155, 15, v44
	v_and_b32_e32 v154, 60, v154
	v_lshl_add_u32 v155, v155, 2, v16
	v_add_u32_e32 v154, v16, v154
	ds_read_b32 v154, v154
	ds_read_b32 v155, v155 offset:64
	v_lshrrev_b32_e32 v156, 2, v45
	v_and_b32_e32 v157, 15, v45
	v_and_b32_e32 v156, 60, v156
	v_lshl_add_u32 v157, v157, 2, v16
	v_add_u32_e32 v156, v16, v156
	ds_read_b32 v156, v156
	ds_read_b32 v157, v157 offset:64
	v_lshrrev_b32_e32 v158, 2, v46
	v_and_b32_e32 v159, 15, v46
	v_and_b32_e32 v158, 60, v158
	v_lshl_add_u32 v159, v159, 2, v16
	v_add_u32_e32 v158, v16, v158
	ds_read_b32 v158, v158
	ds_read_b32 v159, v159 offset:64
	v_lshrrev_b32_e32 v160, 2, v47
	v_and_b32_e32 v161, 15, v47
	v_and_b32_e32 v160, 60, v160
	v_lshl_add_u32 v161, v161, 2, v16
	v_add_u32_e32 v160, v16, v160
	ds_read_b32 v160, v160
	ds_read_b32 v161, v161 offset:64
	v_lshrrev_b32_e32 v162, 2, v48
	v_and_b32_e32 v163, 15, v48
	v_and_b32_e32 v162, 60, v162
	v_lshl_add_u32 v163, v163, 2, v16
	v_add_u32_e32 v162, v16, v162
	ds_read_b32 v162, v162
	ds_read_b32 v163, v163 offset:64
	s_waitcnt lgkmcnt(0)
; #define RT_PK(q_) (ex[q_] | (int)((__float_as_uint(usc[ex[q_]]) >> 23) << 14))
;     __device__ __forceinline__ void fused(f32x4 (&acc)[2][2][4][2], const Unit& u, int wr, int wc, int fr, int fq, PG8_LAS unsigned char* lds, int wid, int lane) const {
;     ...
;             for (int q = 0; q < 16; ++q) { sc[q] = __builtin_amdgcn_exp2f((sc[q] - smax) * 1.4426950408889634f); }
; #pragma unroll
;             for (int q = 0; q < 16; ++q) sum += sc[q];
;             const float rs = 1.0f / sum;
;             asm volatile("s_waitcnt lgkmcnt(0)" ::: "memory");
;             int ex[16];
; #pragma unroll
;             for (int q = 0; q < 16; ++q) { const unsigned cid = __float_as_uint(best[q]) & 255u; ex[q] = idxl[cid >> 4] * 128 + idxl[16 + (cid & 15u)]; }
;             const size_t o = ((size_t)u.pn * 16384 + (size_t)(u.pm * BM + row)) * 16;
;             typedef int i32x4 __attribute__((ext_vector_type(4)));
; #pragma unroll
;             for (int i = 0; i < 4; ++i) {
;     ...
;                 *(i32x4*)(eidx + o + 4 * i) = (i32x4){RT_PK(4 * i), RT_PK(4 * i + 1), RT_PK(4 * i + 2), RT_PK(4 * i + 3)};
;                 *(f32x4*)(egate + o + 4 * i) = (f32x4){sc[4 * i] * rs * vsc[ex[4 * i]], sc[4 * i + 1] * rs * vsc[ex[4 * i + 1]], sc[4 * i + 2] * rs * vsc[ex[4 * i + 2]], sc[4 * i + 3] * rs * vsc[ex[4 * i + 3]]};
	v_lshl_add_u32 v164, v140, 7, v141
	v_ashrrev_i32_e32 v165, 31, v164
	v_lshlrev_b64 v[166:167], 2, v[164:165]
	v_lshl_add_u64 v[168:169], s[8:9], 0, v[166:167]
	global_load_dword v170, v[168:169], off
	v_lshl_add_u64 v[168:169], s[6:7], 0, v[166:167]
	global_load_dword v182, v[168:169], off
	v_lshl_add_u32 v164, v142, 7, v143
	v_ashrrev_i32_e32 v165, 31, v164
	v_lshlrev_b64 v[166:167], 2, v[164:165]
	v_lshl_add_u64 v[168:169], s[8:9], 0, v[166:167]
	global_load_dword v171, v[168:169], off
	v_lshl_add_u64 v[168:169], s[6:7], 0, v[166:167]
	global_load_dword v183, v[168:169], off
	v_lshl_add_u32 v164, v144, 7, v145
	v_ashrrev_i32_e32 v165, 31, v164
	v_lshlrev_b64 v[166:167], 2, v[164:165]
	v_lshl_add_u64 v[168:169], s[8:9], 0, v[166:167]
	global_load_dword v172, v[168:169], off
	v_lshl_add_u64 v[168:169], s[6:7], 0, v[166:167]
	global_load_dword v184, v[168:169], off
	v_lshl_add_u32 v164, v146, 7, v147
	v_ashrrev_i32_e32 v165, 31, v164
	v_lshlrev_b64 v[166:167], 2, v[164:165]
	v_lshl_add_u64 v[168:169], s[8:9], 0, v[166:167]
	global_load_dword v173, v[168:169], off
	v_lshl_add_u64 v[168:169], s[6:7], 0, v[166:167]
	global_load_dword v185, v[168:169], off
	v_lshl_add_u32 v164, v148, 7, v149
	v_ashrrev_i32_e32 v165, 31, v164
	v_lshlrev_b64 v[166:167], 2, v[164:165]
	v_lshl_add_u64 v[168:169], s[8:9], 0, v[166:167]
	global_load_dword v174, v[168:169], off
	v_lshl_add_u64 v[168:169], s[6:7], 0, v[166:167]
	global_load_dword v186, v[168:169], off
	v_lshl_add_u32 v164, v150, 7, v151
	v_ashrrev_i32_e32 v165, 31, v164
	v_lshlrev_b64 v[166:167], 2, v[164:165]
	v_lshl_add_u64 v[168:169], s[8:9], 0, v[166:167]
	global_load_dword v175, v[168:169], off
	v_lshl_add_u64 v[168:169], s[6:7], 0, v[166:167]
	global_load_dword v187, v[168:169], off
	v_lshl_add_u32 v164, v152, 7, v153
	v_ashrrev_i32_e32 v165, 31, v164
	v_lshlrev_b64 v[166:167], 2, v[164:165]
	v_lshl_add_u64 v[168:169], s[8:9], 0, v[166:167]
	global_load_dword v176, v[168:169], off
	v_lshl_add_u64 v[168:169], s[6:7], 0, v[166:167]
	global_load_dword v188, v[168:169], off
	v_lshl_add_u32 v164, v154, 7, v155
	v_ashrrev_i32_e32 v165, 31, v164
	v_lshlrev_b64 v[166:167], 2, v[164:165]
	v_lshl_add_u64 v[168:169], s[8:9], 0, v[166:167]
	global_load_dword v177, v[168:169], off
	v_lshl_add_u64 v[168:169], s[6:7], 0, v[166:167]
	global_load_dword v189, v[168:169], off
	v_lshl_add_u32 v164, v156, 7, v157
	v_ashrrev_i32_e32 v165, 31, v164
	v_lshlrev_b64 v[166:167], 2, v[164:165]
	v_lshl_add_u64 v[168:169], s[8:9], 0, v[166:167]
	global_load_dword v178, v[168:169], off
	v_lshl_add_u64 v[168:169], s[6:7], 0, v[166:167]
	global_load_dword v190, v[168:169], off
	v_lshl_add_u32 v164, v158, 7, v159
	v_ashrrev_i32_e32 v165, 31, v164
	v_lshlrev_b64 v[166:167], 2, v[164:165]
	v_lshl_add_u64 v[168:169], s[8:9], 0, v[166:167]
	global_load_dword v179, v[168:169], off
	v_lshl_add_u64 v[168:169], s[6:7], 0, v[166:167]
	global_load_dword v191, v[168:169], off
	v_lshl_add_u32 v164, v160, 7, v161
	v_ashrrev_i32_e32 v165, 31, v164
	v_lshlrev_b64 v[166:167], 2, v[164:165]
	v_lshl_add_u64 v[168:169], s[8:9], 0, v[166:167]
	global_load_dword v180, v[168:169], off
	v_lshl_add_u64 v[168:169], s[6:7], 0, v[166:167]
	global_load_dword v192, v[168:169], off
	v_lshl_add_u32 v164, v162, 7, v163
	v_ashrrev_i32_e32 v165, 31, v164
	v_lshlrev_b64 v[166:167], 2, v[164:165]
	v_lshl_add_u64 v[168:169], s[8:9], 0, v[166:167]
	global_load_dword v181, v[168:169], off
	v_lshl_add_u64 v[168:169], s[6:7], 0, v[166:167]
	global_load_dword v193, v[168:169], off
	v_and_b32_e32 v8, 0xffffff00, v17
	v_mul_f32_e32 v2, 0x3fb8aa3b, v2
	v_exp_f32_e32 v28, v2
	v_sub_f32_e32 v2, v8, v51
	v_and_b32_e32 v9, 0xffffff00, v39
	v_mul_f32_e32 v2, 0x3fb8aa3b, v2
	v_exp_f32_e32 v29, v2
	v_sub_f32_e32 v2, v9, v51
	v_and_b32_e32 v31, 0xffffff00, v40
	v_mul_f32_e32 v2, 0x3fb8aa3b, v2
	v_exp_f32_e32 v30, v2
	v_sub_f32_e32 v2, v31, v51
	v_and_b32_e32 v32, 0xffffff00, v41
	v_mul_f32_e32 v2, 0x3fb8aa3b, v2
	v_exp_f32_e32 v31, v2
	v_sub_f32_e32 v2, v32, v51
	v_and_b32_e32 v34, 0xffffff00, v42
	v_mul_f32_e32 v2, 0x3fb8aa3b, v2
	v_exp_f32_e32 v6, v2
	v_sub_f32_e32 v2, v34, v51
	v_and_b32_e32 v35, 0xffffff00, v43
	v_mul_f32_e32 v2, 0x3fb8aa3b, v2
	v_exp_f32_e32 v7, v2
	v_sub_f32_e32 v2, v35, v51
	v_mul_f32_e32 v2, 0x3fb8aa3b, v2
	v_exp_f32_e32 v8, v2
	v_lshl_or_b32 v2, s18, 8, v128
	v_ashrrev_i32_e32 v3, 31, v2
	s_lshl_b64 s[4:5], s[16:17], 18
	v_lshl_add_u64 v[32:33], v[2:3], 4, s[4:5]
	s_mov_b32 s4, 0x7fc000
	v_sub_f32_e32 v24, v51, v51
	v_mul_f32_e32 v24, 0x3fb8aa3b, v24
	v_exp_f32_e32 v24, v24
	s_waitcnt vmcnt(28)
; #define RT_PK(q_) (ex[q_] | (int)((__float_as_uint(usc[ex[q_]]) >> 23) << 14))
;     __device__ __forceinline__ void fused(f32x4 (&acc)[2][2][4][2], const Unit& u, int wr, int wc, int fr, int fq, PG8_LAS unsigned char* lds, int wid, int lane) const {
;     ...
;             for (int q = 0; q < 16; ++q) { sc[q] = __builtin_amdgcn_exp2f((sc[q] - smax) * 1.4426950408889634f); }
; #pragma unroll
;             for (int q = 0; q < 16; ++q) sum += sc[q];
;             const float rs = 1.0f / sum;
;             asm volatile("s_waitcnt lgkmcnt(0)" ::: "memory");
;             int ex[16];
; #pragma unroll
;             for (int q = 0; q < 16; ++q) { const unsigned cid = __float_as_uint(best[q]) & 255u; ex[q] = idxl[cid >> 4] * 128 + idxl[16 + (cid & 15u)]; }
;             const size_t o = ((size_t)u.pn * 16384 + (size_t)(u.pm * BM + row)) * 16;
;             typedef int i32x4 __attribute__((ext_vector_type(4)));
; #pragma unroll
;             for (int i = 0; i < 4; ++i) {
;     ...
;                 *(i32x4*)(eidx + o + 4 * i) = (i32x4){RT_PK(4 * i), RT_PK(4 * i + 1), RT_PK(4 * i + 2), RT_PK(4 * i + 3)};
;                 *(f32x4*)(egate + o + 4 * i) = (f32x4){sc[4 * i] * rs * vsc[ex[4 * i]], sc[4 * i + 1] * rs * vsc[ex[4 * i + 1]], sc[4 * i + 2] * rs * vsc[ex[4 * i + 2]], sc[4 * i + 3] * rs * vsc[ex[4 * i + 3]]};
	v_lshrrev_b32_e32 v1, 9, v1
	v_and_or_b32 v2, v1, s4, v0
	v_and_b32_e32 v36, 0xffffff00, v44
	v_and_b32_e32 v37, 0xffffff00, v45
	v_and_b32_e32 v49, 0xffffff00, v46
	v_and_b32_e32 v50, 0xffffff00, v47
	v_and_b32_e32 v52, 0xffffff00, v48
	v_lshrrev_b32_e32 v0, 9, v5
	v_and_or_b32 v3, v0, s4, v4
	v_lshrrev_b32_e32 v0, 9, v11
	v_and_or_b32 v4, v0, s4, v10
	v_lshrrev_b32_e32 v0, 9, v13
	v_and_or_b32 v5, v0, s4, v12
	v_lshlrev_b64 v[12:13], 2, v[32:33]
	v_lshl_add_u64 v[0:1], s[12:13], 0, v[12:13]
	global_store_dwordx4 v[0:1], v[2:5], off
	v_lshrrev_b32_e32 v32, 2, v40
	v_add_f32_e32 v10, 0, v24
	v_add_f32_e32 v10, v25, v10
	v_add_f32_e32 v10, v26, v10
	v_add_f32_e32 v10, v27, v10
	v_sub_f32_e32 v2, v36, v51
	v_add_f32_e32 v10, v28, v10
	v_mul_f32_e32 v2, 0x3fb8aa3b, v2
	v_add_f32_e32 v10, v29, v10
	v_exp_f32_e32 v9, v2
	v_sub_f32_e32 v2, v37, v51
	v_add_f32_e32 v10, v30, v10
	v_mul_f32_e32 v2, 0x3fb8aa3b, v2
	v_sub_f32_e32 v3, v49, v51
	v_add_f32_e32 v10, v31, v10
	v_exp_f32_e32 v2, v2
	v_mul_f32_e32 v3, 0x3fb8aa3b, v3
	v_sub_f32_e32 v4, v50, v51
	v_add_f32_e32 v10, v6, v10
	v_exp_f32_e32 v3, v3
	v_mul_f32_e32 v4, 0x3fb8aa3b, v4
	v_sub_f32_e32 v5, v52, v51
	v_add_f32_e32 v10, v7, v10
	v_exp_f32_e32 v4, v4
	v_mul_f32_e32 v5, 0x3fb8aa3b, v5
	v_add_f32_e32 v10, v8, v10
	v_exp_f32_e32 v5, v5
	v_add_f32_e32 v10, v9, v10
	v_add_f32_e32 v10, v2, v10
	v_lshrrev_b32_e32 v11, 2, v38
	v_lshrrev_b32_e32 v15, 2, v17
	v_add_f32_e32 v10, v3, v10
	v_and_b32_e32 v11, 60, v11
	v_and_b32_e32 v14, 15, v38
	v_and_b32_e32 v15, 60, v15
	v_and_b32_e32 v17, 15, v17
	v_lshrrev_b32_e32 v22, 2, v39
	v_and_b32_e32 v23, 15, v39
	v_and_b32_e32 v33, 15, v40
	v_add_f32_e32 v10, v4, v10
	v_add_u32_e32 v11, v16, v11
	v_lshl_add_u32 v14, v14, 2, v16
	v_add_u32_e32 v15, v16, v15
	v_lshl_add_u32 v17, v17, 2, v16
	v_and_b32_e32 v22, 60, v22
	v_lshl_add_u32 v23, v23, 2, v16
	v_and_b32_e32 v32, 60, v32
	v_lshl_add_u32 v33, v33, 2, v16
	v_add_f32_e32 v10, v5, v10
	v_add_u32_e32 v22, v16, v22
	v_add_u32_e32 v32, v16, v32
	ds_read_b32 v11, v11
	ds_read_b32 v14, v14 offset:64
	ds_read_b32 v15, v15
	ds_read_b32 v17, v17 offset:64
	ds_read_b32 v34, v22
	ds_read_b32 v23, v23 offset:64
	ds_read_b32 v35, v32
	ds_read_b32 v33, v33 offset:64
	s_waitcnt lgkmcnt(6)
	v_lshl_add_u32 v14, v11, 7, v14
	v_div_scale_f32 v11, s[16:17], v10, v10, 1.0
	v_rcp_f32_e32 v36, v11
	s_waitcnt lgkmcnt(4)
	v_lshl_add_u32 v22, v15, 7, v17
	s_waitcnt lgkmcnt(2)
	v_lshl_add_u32 v32, v34, 7, v23
	s_waitcnt lgkmcnt(0)
	v_lshl_add_u32 v34, v35, 7, v33
	v_fma_f32 v15, -v11, v36, 1.0
	v_fmac_f32_e32 v36, v15, v36
	v_div_scale_f32 v15, vcc, 1.0, v10, 1.0
	v_mul_f32_e32 v17, v15, v36
	v_fma_f32 v23, -v11, v17, v15
	v_fmac_f32_e32 v17, v23, v36
	v_fma_f32 v11, -v11, v17, v15
	v_div_fmas_f32 v11, v11, v36, v17
	v_div_fixup_f32 v10, v11, v10, 1.0
	v_pk_mul_f32 v[24:25], v[24:25], v[10:11] op_sel_hi:[1,0]
	v_pk_mul_f32 v[26:27], v[26:27], v[10:11] op_sel_hi:[1,0]
	v_ashrrev_i32_e32 v15, 31, v14
	v_ashrrev_i32_e32 v33, 31, v32
	v_lshl_add_u64 v[12:13], s[10:11], 0, v[12:13]
	v_ashrrev_i32_e32 v23, 31, v22
	v_lshlrev_b64 v[36:37], 2, v[32:33]
	v_lshl_add_u64 v[38:39], s[8:9], 0, v[36:37]
	v_ashrrev_i32_e32 v35, 31, v34
	s_waitcnt vmcnt(1)
	v_pk_mul_f32 v[18:19], v[24:25], v[194:195]
	v_lshlrev_b64 v[24:25], 2, v[14:15]
	v_pk_mul_f32 v[20:21], v[26:27], v[196:197]
	global_store_dwordx4 v[12:13], v[18:21], off
	v_lshlrev_b64 v[26:27], 2, v[22:23]
	s_nop 0
	v_lshl_add_u64 v[18:19], s[8:9], 0, v[24:25]
	v_lshl_add_u64 v[20:21], s[8:9], 0, v[26:27]
	v_lshlrev_b64 v[38:39], 2, v[34:35]
	v_lshl_add_u64 v[18:19], s[8:9], 0, v[38:39]
	v_lshrrev_b32_e32 v11, 9, v170
	v_and_or_b32 v18, v11, s4, v14
	v_lshrrev_b32_e32 v11, 9, v171
	v_and_or_b32 v19, v11, s4, v22
	v_lshrrev_b32_e32 v11, 9, v172
	v_and_or_b32 v20, v11, s4, v32
	v_lshrrev_b32_e32 v11, 9, v173
	v_and_or_b32 v21, v11, s4, v34
	global_store_dwordx4 v[0:1], v[18:21], off offset:16
	v_lshrrev_b32_e32 v11, 2, v41
	v_lshrrev_b32_e32 v15, 2, v42
	v_lshrrev_b32_e32 v18, 2, v43
	v_lshrrev_b32_e32 v20, 2, v44
	v_and_b32_e32 v11, 60, v11
	v_and_b32_e32 v14, 15, v41
	v_and_b32_e32 v15, 60, v15
	v_and_b32_e32 v17, 15, v42
	v_and_b32_e32 v18, 60, v18
	v_and_b32_e32 v19, 15, v43
	v_and_b32_e32 v20, 60, v20
	v_and_b32_e32 v21, 15, v44
	v_add_u32_e32 v11, v16, v11
	v_lshl_add_u32 v14, v14, 2, v16
	v_add_u32_e32 v15, v16, v15
	v_lshl_add_u32 v17, v17, 2, v16
	v_add_u32_e32 v18, v16, v18
	v_lshl_add_u32 v19, v19, 2, v16
	v_add_u32_e32 v20, v16, v20
	v_lshl_add_u32 v21, v21, 2, v16
	ds_read_b32 v11, v11
	ds_read_b32 v14, v14 offset:64
	ds_read_b32 v15, v15
	ds_read_b32 v17, v17 offset:64
	ds_read_b32 v18, v18
	ds_read_b32 v19, v19 offset:64
	ds_read_b32 v20, v20
	ds_read_b32 v21, v21 offset:64
	s_waitcnt lgkmcnt(6)
; #define RT_PK(q_) (ex[q_] | (int)((__float_as_uint(usc[ex[q_]]) >> 23) << 14))
;     __device__ __forceinline__ void fused(f32x4 (&acc)[2][2][4][2], const Unit& u, int wr, int wc, int fr, int fq, PG8_LAS unsigned char* lds, int wid, int lane) const {
;     ...
;             for (int q = 0; q < 16; ++q) { const unsigned cid = __float_as_uint(best[q]) & 255u; ex[q] = idxl[cid >> 4] * 128 + idxl[16 + (cid & 15u)]; }
;             const size_t o = ((size_t)u.pn * 16384 + (size_t)(u.pm * BM + row)) * 16;
;             typedef int i32x4 __attribute__((ext_vector_type(4)));
; #pragma unroll
;             for (int i = 0; i < 4; ++i) {
;     ...
;                 *(i32x4*)(eidx + o + 4 * i) = (i32x4){RT_PK(4 * i), RT_PK(4 * i + 1), RT_PK(4 * i + 2), RT_PK(4 * i + 3)};
;                 *(f32x4*)(egate + o + 4 * i) = (f32x4){sc[4 * i] * rs * vsc[ex[4 * i]], sc[4 * i + 1] * rs * vsc[ex[4 * i + 1]], sc[4 * i + 2] * rs * vsc[ex[4 * i + 2]], sc[4 * i + 3] * rs * vsc[ex[4 * i + 3]]};
	v_lshl_add_u32 v14, v11, 7, v14
	s_waitcnt lgkmcnt(4)
	v_lshl_add_u32 v22, v15, 7, v17
	s_waitcnt lgkmcnt(2)
	v_lshl_add_u32 v32, v18, 7, v19
	v_pk_mul_f32 v[18:19], v[28:29], v[10:11] op_sel_hi:[1,0]
	s_waitcnt lgkmcnt(0)
	v_lshl_add_u32 v34, v20, 7, v21
	v_pk_mul_f32 v[20:21], v[30:31], v[10:11] op_sel_hi:[1,0]
	v_ashrrev_i32_e32 v15, 31, v14
	v_ashrrev_i32_e32 v33, 31, v32
	v_ashrrev_i32_e32 v23, 31, v22
	v_lshlrev_b64 v[28:29], 2, v[32:33]
	v_lshl_add_u64 v[30:31], s[8:9], 0, v[28:29]
	v_ashrrev_i32_e32 v35, 31, v34
	v_pk_mul_f32 v[20:21], v[20:21], v[184:185]
	v_pk_mul_f32 v[18:19], v[18:19], v[182:183]
	v_lshlrev_b64 v[24:25], 2, v[14:15]
	global_store_dwordx4 v[12:13], v[18:21], off offset:16
	v_lshlrev_b64 v[26:27], 2, v[22:23]
	s_nop 0
	v_lshl_add_u64 v[18:19], s[8:9], 0, v[24:25]
	v_lshl_add_u64 v[20:21], s[8:9], 0, v[26:27]
	v_lshlrev_b64 v[30:31], 2, v[34:35]
	v_lshl_add_u64 v[18:19], s[8:9], 0, v[30:31]
	v_lshrrev_b32_e32 v11, 9, v174
	v_and_or_b32 v18, v11, s4, v14
	v_lshrrev_b32_e32 v11, 9, v175
	v_and_or_b32 v19, v11, s4, v22
	v_lshrrev_b32_e32 v11, 9, v176
	v_and_or_b32 v20, v11, s4, v32
	v_lshrrev_b32_e32 v11, 9, v177
	v_and_or_b32 v21, v11, s4, v34
	global_store_dwordx4 v[0:1], v[18:21], off offset:32
	v_lshrrev_b32_e32 v11, 2, v45
	v_lshrrev_b32_e32 v15, 2, v46
	v_lshrrev_b32_e32 v18, 2, v47
	v_lshrrev_b32_e32 v20, 2, v48
	v_and_b32_e32 v11, 60, v11
	v_and_b32_e32 v14, 15, v45
	v_and_b32_e32 v15, 60, v15
	v_and_b32_e32 v17, 15, v46
	v_and_b32_e32 v18, 60, v18
	v_and_b32_e32 v19, 15, v47
	v_and_b32_e32 v20, 60, v20
	v_add_u32_e32 v11, v16, v11
	v_lshl_add_u32 v14, v14, 2, v16
	v_add_u32_e32 v15, v16, v15
	v_lshl_add_u32 v17, v17, 2, v16
	v_add_u32_e32 v18, v16, v18
	v_lshl_add_u32 v19, v19, 2, v16
	v_add_u32_e32 v20, v16, v20
	v_and_b32_e32 v21, 15, v48
	v_lshl_add_u32 v16, v21, 2, v16
	ds_read_b32 v11, v11
	ds_read_b32 v14, v14 offset:64
	ds_read_b32 v15, v15
	ds_read_b32 v17, v17 offset:64
	ds_read_b32 v18, v18
	ds_read_b32 v19, v19 offset:64
	ds_read_b32 v20, v20
	ds_read_b32 v21, v16 offset:64
	s_waitcnt lgkmcnt(6)
	v_lshl_add_u32 v14, v11, 7, v14
	s_waitcnt lgkmcnt(4)
	v_lshl_add_u32 v16, v15, 7, v17
	s_waitcnt lgkmcnt(2)
	v_lshl_add_u32 v18, v18, 7, v19
	v_pk_mul_f32 v[6:7], v[6:7], v[10:11] op_sel_hi:[1,0]
	v_pk_mul_f32 v[8:9], v[8:9], v[10:11] op_sel_hi:[1,0]
	v_ashrrev_i32_e32 v15, 31, v14
	v_ashrrev_i32_e32 v19, 31, v18
	s_waitcnt lgkmcnt(0)
	v_lshl_add_u32 v20, v20, 7, v21
	v_lshlrev_b64 v[22:23], 2, v[14:15]
	v_ashrrev_i32_e32 v17, 31, v16
	v_ashrrev_i32_e32 v21, 31, v20
	v_pk_mul_f32 v[8:9], v[8:9], v[188:189]
	v_pk_mul_f32 v[6:7], v[6:7], v[186:187]
	v_lshlrev_b64 v[26:27], 2, v[18:19]
	global_store_dwordx4 v[12:13], v[6:9], off offset:32
	v_lshlrev_b64 v[24:25], 2, v[16:17]
	v_lshl_add_u64 v[28:29], s[8:9], 0, v[26:27]
	v_lshl_add_u64 v[6:7], s[8:9], 0, v[22:23]
	v_lshl_add_u64 v[8:9], s[8:9], 0, v[24:25]
	v_lshlrev_b64 v[28:29], 2, v[20:21]
	v_lshl_add_u64 v[6:7], s[8:9], 0, v[28:29]
	v_lshrrev_b32_e32 v6, 9, v178
	v_lshrrev_b32_e32 v7, 9, v179
	v_lshrrev_b32_e32 v8, 9, v180
	v_and_or_b32 v6, v6, s4, v14
	v_and_or_b32 v7, v7, s4, v16
	v_lshrrev_b32_e32 v9, 9, v181
	v_and_or_b32 v8, v8, s4, v18
	v_and_or_b32 v9, v9, s4, v20
	global_store_dwordx4 v[0:1], v[6:9], off offset:48
	v_pk_mul_f32 v[0:1], v[2:3], v[10:11] op_sel_hi:[1,0]
	v_pk_mul_f32 v[2:3], v[4:5], v[10:11] op_sel_hi:[1,0]
	v_pk_mul_f32 v[0:1], v[0:1], v[190:191]
	v_pk_mul_f32 v[2:3], v[2:3], v[192:193]
	global_store_dwordx4 v[12:13], v[0:3], off offset:48

; #define PG8_LAS __attribute__((address_space(3)))
;     __device__ __forceinline__ void fused(f32x4 (&acc)[2][2][4][2], const Unit& u, int wr, int wc, int fr, int fq, PG8_LAS unsigned char* lds, int wid, int lane) const {
;     ...
;         if (half == 0) {
;             PG8_LAS int* idxl = (PG8_LAS int*)(lds + 65536) + row * 32;
;             float v0[16], v1[16];
; #pragma unroll
;             for (int q = 0; q < 16; ++q) { const unsigned b0 = __float_as_uint(top0[q]), b1 = __float_as_uint(top1[q]);
;                 v0[q] = __uint_as_float(b0 & ~127u); v1[q] = __uint_as_float(b1 & ~127u); idxl[q] = (int)(b0 & 127u); idxl[16 + q] = (int)(b1 & 127u); }
;             float best[16];
;             { float cv[16]; cv[0] = __uint_as_float((__float_as_uint(v0[0] + v1[0]) & ~255u) | 0u); cv[1] = __uint_as_float((__float_as_uint(v0[0] + v1[1]) & ~255u) | 1u); cv[2] = __uint_as_float((__float_as_uint(v0[0] + v1[2]) & ~255u) | 2u); cv[3] = __uint_as_float((__float_as_uint(v0[0] + v1[3]) & ~255u) | 3u); cv[4] = __uint_as_float((__float_as_uint(v0[0] + v1[4]) & ~255u) | 4u); cv[5] = __uint_as_float((__float_as_uint(v0[0] + v1[5]) & ~255u) | 5u); cv[6] = __uint_as_float((__float_as_uint(v0[0] + v1[6]) & ~255u) | 6u); cv[7] = __uint_as_float((__float_as_uint(v0[0] + v1[7]) & ~255u) | 7u); cv[8] = __uint_as_float((__float_as_uint(v0[0] + v1[8]) & ~255u) | 8u); cv[9] = __uint_as_float((__float_as_uint(v0[0] + v1[9]) & ~255u) | 9u); cv[10] = __uint_as_float((__float_as_uint(v0[0] + v1[10]) & ~255u) | 10u); cv[11] = __uint_as_float((__float_as_uint(v0[0] + v1[11]) & ~255u) | 11u); cv[12] = __uint_as_float((__float_as_uint(v0[0] + v1[12]) & ~255u) | 12u); cv[13] = __uint_as_float((__float_as_uint(v0[0] + v1[13]) & ~255u) | 13u); cv[14] = __uint_as_float((__float_as_uint(v0[0] + v1[14]) & ~255u) | 14u); cv[15] = __uint_as_float((__float_as_uint(v0[0] + v1[15]) & ~255u) | 15u); sort16_desc(cv);
; #pragma unroll
;               for (int q = 0; q < 16; ++q) best[q] = cv[q]; }
.LBB0_606:
	s_waitcnt lgkmcnt(0)
	s_barrier
	s_and_b64 vcc, exec, s[4:5]
	s_cbranch_vccnz .LBB0_608
	v_lshl_add_u32 v16, v128, 7, 0
	v_add_u32_e32 v16, 0x10000, v16
	v_and_b32_e32 v17, 0xffffff80, v12
	v_and_b32_e32 v18, 0xffffff80, v13
	v_and_b32_e32 v21, 0x7f, v77
	v_and_b32_e32 v20, 0x7f, v76
	v_and_b32_e32 v13, 0x7f, v13
	v_and_b32_e32 v12, 0x7f, v12
	v_and_b32_e32 v26, 0xffffff80, v14
	v_and_b32_e32 v28, 0xffffff80, v15
	v_and_b32_e32 v23, 0x7f, v79
	v_and_b32_e32 v22, 0x7f, v78
	v_and_b32_e32 v15, 0x7f, v15
	v_and_b32_e32 v14, 0x7f, v14
	ds_write_b128 v16, v[20:23]
	ds_write_b128 v16, v[12:15] offset:64
	v_and_b32_e32 v21, 0xffffff80, v8
	v_and_b32_e32 v23, 0xffffff80, v9
	v_and_b32_e32 v13, 0x7f, v73
	v_and_b32_e32 v12, 0x7f, v72
	v_and_b32_e32 v9, 0x7f, v9
	v_and_b32_e32 v8, 0x7f, v8
	v_and_b32_e32 v30, 0xffffff80, v10
	v_and_b32_e32 v32, 0xffffff80, v11
	v_and_b32_e32 v15, 0x7f, v75
	v_and_b32_e32 v14, 0x7f, v74
	v_and_b32_e32 v11, 0x7f, v11
	v_and_b32_e32 v10, 0x7f, v10
	v_and_b32_e32 v19, 0xffffff80, v76
	ds_write_b128 v16, v[12:15] offset:16
	ds_write_b128 v16, v[8:11] offset:80
	v_and_b32_e32 v13, 0xffffff80, v4
	v_and_b32_e32 v15, 0xffffff80, v5
	v_and_b32_e32 v9, 0x7f, v69
	v_and_b32_e32 v8, 0x7f, v68
	v_and_b32_e32 v5, 0x7f, v5
	v_and_b32_e32 v4, 0x7f, v4
	v_and_b32_e32 v34, 0xffffff80, v6
	v_and_b32_e32 v36, 0xffffff80, v7
	v_and_b32_e32 v11, 0x7f, v71
	v_and_b32_e32 v10, 0x7f, v70
	v_and_b32_e32 v7, 0x7f, v7
	v_and_b32_e32 v6, 0x7f, v6
	ds_write_b128 v16, v[8:11] offset:32
	ds_write_b128 v16, v[4:7] offset:96
	v_and_b32_e32 v5, 0x7f, v65
	v_and_b32_e32 v4, 0x7f, v64
	v_and_b32_e32 v41, 0xffffff80, v2
	v_and_b32_e32 v42, 0xffffff80, v3
	v_and_b32_e32 v7, 0x7f, v67
	v_and_b32_e32 v6, 0x7f, v66
	v_and_b32_e32 v11, 0x7f, v3
	v_and_b32_e32 v10, 0x7f, v2
	v_add_f32_e32 v2, v19, v17
	s_movk_i32 s3, 0xff00
	v_add_f32_e32 v3, v19, v18
	v_and_b32_e32 v24, 0xffffff80, v77
	ds_write_b128 v16, v[4:7] offset:48
	v_and_b32_e32 v2, 0xffffff00, v2
	v_and_or_b32 v3, v3, s3, 1
	v_add_f32_e32 v4, v19, v26
	v_add_f32_e32 v5, v19, v28
	v_and_b32_e32 v40, 0xffffff80, v1
	v_and_b32_e32 v9, 0x7f, v1
	v_and_b32_e32 v8, 0x7f, v0
	v_and_or_b32 v4, v4, s3, 2
	v_and_or_b32 v5, v5, s3, 3
	v_add_f32_e32 v48, v24, v17
	v_add_f32_e32 v49, v24, v18
	ds_write_b128 v16, v[8:11] offset:112
	v_add_f32_e32 v6, v19, v21
	v_add_f32_e32 v7, v19, v23
	v_add_f32_e32 v11, v19, v15
	v_add_f32_e32 v15, v19, v36
	v_add_f32_e32 v36, v19, v40
	v_max_f32_e32 v40, v2, v3
	v_min_f32_e32 v2, v2, v3
	v_max_f32_e32 v3, v5, v5
	v_and_or_b32 v48, v48, s3, 16
	v_and_or_b32 v49, v49, s3, 17
	v_add_f32_e32 v50, v24, v26
	v_add_f32_e32 v51, v24, v28
	v_and_or_b32 v6, v6, s3, 4
	v_and_or_b32 v7, v7, s3, 5
	v_add_f32_e32 v8, v19, v30
	v_add_f32_e32 v9, v19, v32
	v_max_f32_e32 v5, v4, v3
	v_min_f32_e32 v3, v4, v3
	v_and_or_b32 v50, v50, s3, 18
	v_and_or_b32 v51, v51, s3, 19
	v_and_or_b32 v8, v8, s3, 6
	v_and_or_b32 v9, v9, s3, 7
	v_max_f32_e32 v4, v40, v5
	v_min_f32_e32 v5, v40, v5
	v_max_f32_e32 v40, v2, v3
	v_add_f32_e32 v52, v24, v21
	v_add_f32_e32 v23, v24, v23
	v_add_f32_e32 v30, v24, v30
	v_add_f32_e32 v24, v24, v32
	v_max_f32_e32 v58, v48, v49
	v_min_f32_e32 v48, v48, v49
	v_max_f32_e32 v49, v51, v51
	v_min_f32_e32 v2, v2, v3
	v_max_f32_e32 v3, v40, v5
	v_min_f32_e32 v5, v40, v5
	v_max_f32_e32 v40, v6, v7
	v_min_f32_e32 v6, v6, v7
	v_max_f32_e32 v7, v9, v9
	v_and_or_b32 v52, v52, s3, 20
	v_and_or_b32 v23, v23, s3, 21
	v_and_or_b32 v30, v30, s3, 22
	v_and_or_b32 v24, v24, s3, 23
	v_max_f32_e32 v51, v50, v49
	v_min_f32_e32 v49, v50, v49
	v_max_f32_e32 v9, v8, v7
	v_min_f32_e32 v7, v8, v7
	v_max_f32_e32 v50, v58, v51
	v_min_f32_e32 v51, v58, v51
	v_max_f32_e32 v58, v48, v49
	v_max_f32_e32 v8, v40, v9
	v_min_f32_e32 v9, v40, v9
	v_max_f32_e32 v40, v6, v7
	v_min_f32_e32 v48, v48, v49
	v_max_f32_e32 v49, v58, v51
	v_min_f32_e32 v51, v58, v51
	v_max_f32_e32 v58, v52, v23
	v_min_f32_e32 v23, v52, v23
	v_max_f32_e32 v52, v30, v24
	v_min_f32_e32 v24, v30, v24
	v_min_f32_e32 v6, v6, v7
	v_max_f32_e32 v7, v40, v9
	v_min_f32_e32 v9, v40, v9
	v_max_f32_e32 v30, v58, v52
	v_min_f32_e32 v52, v58, v52
	v_max_f32_e32 v58, v23, v24
	v_max_f32_e32 v40, v4, v8
	v_min_f32_e32 v4, v4, v8
	v_max_f32_e32 v8, v5, v9
	v_min_f32_e32 v23, v23, v24
	v_max_f32_e32 v24, v58, v52
	v_min_f32_e32 v52, v58, v52
	v_and_b32_e32 v25, 0xffffff80, v78
	v_add_f32_e32 v10, v19, v13
	v_min_f32_e32 v5, v5, v9
	v_max_f32_e32 v9, v8, v4
	v_min_f32_e32 v4, v8, v4
	v_max_f32_e32 v8, v3, v7
	v_min_f32_e32 v3, v3, v7
	v_max_f32_e32 v7, v2, v6
	v_max_f32_e32 v58, v50, v30
	v_min_f32_e32 v30, v50, v30
	v_max_f32_e32 v50, v51, v52
	v_and_or_b32 v10, v10, s3, 8
	v_and_or_b32 v11, v11, s3, 9
	v_add_f32_e32 v13, v19, v34
	v_min_f32_e32 v2, v2, v6
	v_max_f32_e32 v6, v7, v3
	v_min_f32_e32 v3, v7, v3
	v_add_f32_e32 v32, v25, v17
	v_add_f32_e32 v53, v25, v18
	v_min_f32_e32 v51, v51, v52
	v_max_f32_e32 v52, v50, v30
	v_min_f32_e32 v30, v50, v30
	v_max_f32_e32 v50, v49, v24
	v_min_f32_e32 v24, v49, v24
	v_max_f32_e32 v49, v48, v23
	v_and_or_b32 v13, v13, s3, 10
	v_and_or_b32 v15, v15, s3, 11
	v_max_f32_e32 v7, v8, v9
	v_min_f32_e32 v8, v8, v9
	v_max_f32_e32 v9, v6, v4
	v_min_f32_e32 v4, v6, v4
	v_max_f32_e32 v6, v3, v5
	v_min_f32_e32 v3, v3, v5
	v_max_f32_e32 v5, v11, v11
	v_and_or_b32 v32, v32, s3, 32
	v_and_or_b32 v53, v53, s3, 33
	v_add_f32_e32 v54, v25, v26
	v_add_f32_e32 v55, v25, v28
	v_min_f32_e32 v23, v48, v23
	v_max_f32_e32 v48, v49, v24
	v_min_f32_e32 v24, v49, v24
	v_and_b32_e32 v27, 0xffffff80, v79
	v_and_b32_e32 v38, 0xffffff80, v0
	v_max_f32_e32 v11, v10, v5
	v_min_f32_e32 v5, v10, v5
	v_max_f32_e32 v10, v15, v15
;     __device__ __forceinline__ void fused(f32x4 (&acc)[2][2][4][2], const Unit& u, int wr, int wc, int fr, int fq, PG8_LAS unsigned char* lds, int wid, int lane) const {
;     ...
;             { float cv[16]; cv[0] = __uint_as_float((__float_as_uint(v0[0] + v1[0]) & ~255u) | 0u); cv[1] = __uint_as_float((__float_as_uint(v0[0] + v1[1]) & ~255u) | 1u); cv[2] = __uint_as_float((__float_as_uint(v0[0] + v1[2]) & ~255u) | 2u); cv[3] = __uint_as_float((__float_as_uint(v0[0] + v1[3]) & ~255u) | 3u); cv[4] = __uint_as_float((__float_as_uint(v0[0] + v1[4]) & ~255u) | 4u); cv[5] = __uint_as_float((__float_as_uint(v0[0] + v1[5]) & ~255u) | 5u); cv[6] = __uint_as_float((__float_as_uint(v0[0] + v1[6]) & ~255u) | 6u); cv[7] = __uint_as_float((__float_as_uint(v0[0] + v1[7]) & ~255u) | 7u); cv[8] = __uint_as_float((__float_as_uint(v0[0] + v1[8]) & ~255u) | 8u); cv[9] = __uint_as_float((__float_as_uint(v0[0] + v1[9]) & ~255u) | 9u); cv[10] = __uint_as_float((__float_as_uint(v0[0] + v1[10]) & ~255u) | 10u); cv[11] = __uint_as_float((__float_as_uint(v0[0] + v1[11]) & ~255u) | 11u); cv[12] = __uint_as_float((__float_as_uint(v0[0] + v1[12]) & ~255u) | 12u); cv[13] = __uint_as_float((__float_as_uint(v0[0] + v1[13]) & ~255u) | 13u); cv[14] = __uint_as_float((__float_as_uint(v0[0] + v1[14]) & ~255u) | 14u); cv[15] = __uint_as_float((__float_as_uint(v0[0] + v1[15]) & ~255u) | 15u); sort16_desc(cv);
; #pragma unroll
;               for (int q = 0; q < 16; ++q) best[q] = cv[q]; }
	v_and_or_b32 v54, v54, s3, 34
	v_and_or_b32 v55, v55, s3, 35
	v_max_f32_e32 v49, v50, v52
	v_min_f32_e32 v50, v50, v52
	v_max_f32_e32 v52, v48, v30
	v_min_f32_e32 v30, v48, v30
	v_max_f32_e32 v48, v24, v51
	v_min_f32_e32 v24, v24, v51
	v_max_f32_e32 v51, v53, v53
	v_add_f32_e32 v34, v19, v38
	v_max_f32_e32 v15, v13, v10
	v_min_f32_e32 v10, v13, v10
	v_add_f32_e32 v21, v25, v21
	v_add_f32_e32 v25, v27, v17
	v_max_f32_e32 v53, v32, v51
	v_min_f32_e32 v32, v32, v51
	v_max_f32_e32 v51, v55, v55
	v_and_or_b32 v34, v34, s3, 12
	v_and_or_b32 v36, v36, s3, 13
	v_add_f32_e32 v38, v19, v41
	v_add_f32_e32 v19, v19, v42
	v_max_f32_e32 v13, v11, v15
	v_min_f32_e32 v11, v11, v15
	v_max_f32_e32 v15, v5, v10
	v_and_or_b32 v21, v21, s3, 36
	v_and_or_b32 v25, v25, s3, 48
	v_add_f32_e32 v56, v27, v18
	v_add_f32_e32 v57, v27, v26
	v_max_f32_e32 v55, v54, v51
	v_min_f32_e32 v51, v54, v51
	v_and_or_b32 v38, v38, s3, 14
	v_and_or_b32 v19, v19, s3, 15
	v_min_f32_e32 v5, v5, v10
	v_max_f32_e32 v10, v15, v11
	v_min_f32_e32 v11, v15, v11
	v_max_f32_e32 v15, v36, v36
	v_and_or_b32 v56, v56, s3, 49
	v_and_or_b32 v57, v57, s3, 50
	v_max_f32_e32 v54, v53, v55
	v_min_f32_e32 v53, v53, v55
	v_max_f32_e32 v55, v32, v51
	v_max_f32_e32 v36, v34, v15
	v_min_f32_e32 v15, v34, v15
	v_max_f32_e32 v34, v38, v38
	v_min_f32_e32 v32, v32, v51
	v_max_f32_e32 v51, v55, v53
	v_min_f32_e32 v53, v55, v53
	v_max_f32_e32 v55, v21, v25
	v_min_f32_e32 v21, v21, v25
	v_max_f32_e32 v25, v57, v57
	v_max_f32_e32 v38, v34, v19
	v_min_f32_e32 v19, v34, v19
	v_max_f32_e32 v57, v56, v25
	v_min_f32_e32 v25, v56, v25
	v_max_f32_e32 v34, v36, v38
	v_min_f32_e32 v36, v36, v38
	v_max_f32_e32 v38, v15, v19
	v_max_f32_e32 v56, v55, v57
	v_min_f32_e32 v55, v55, v57
	v_max_f32_e32 v57, v21, v25
	v_min_f32_e32 v15, v15, v19
	v_max_f32_e32 v19, v38, v36
	v_min_f32_e32 v36, v38, v36
	v_min_f32_e32 v21, v21, v25
	v_max_f32_e32 v25, v57, v55
	v_min_f32_e32 v55, v57, v55
	v_max_f32_e32 v38, v13, v34
	v_min_f32_e32 v13, v13, v34
	v_max_f32_e32 v34, v11, v36
	v_max_f32_e32 v57, v54, v56
	v_min_f32_e32 v54, v54, v56
	v_max_f32_e32 v56, v53, v55
	v_min_f32_e32 v11, v11, v36
	v_max_f32_e32 v36, v34, v13
	v_min_f32_e32 v13, v34, v13
	v_max_f32_e32 v34, v10, v19
	v_min_f32_e32 v10, v10, v19
	v_max_f32_e32 v19, v5, v15
	v_min_f32_e32 v53, v53, v55
	v_max_f32_e32 v55, v56, v54
	v_min_f32_e32 v54, v56, v54
	v_max_f32_e32 v56, v51, v25
	v_min_f32_e32 v25, v51, v25
	v_max_f32_e32 v51, v32, v21
	v_min_f32_e32 v5, v5, v15
	v_max_f32_e32 v15, v19, v10
	v_min_f32_e32 v21, v32, v21
	v_max_f32_e32 v32, v51, v25
	v_min_f32_e32 v10, v19, v10
	v_max_f32_e32 v19, v34, v36
	v_min_f32_e32 v34, v34, v36
	v_max_f32_e32 v36, v15, v13
	v_min_f32_e32 v13, v15, v13
	v_min_f32_e32 v25, v51, v25
	v_max_f32_e32 v51, v56, v55
	v_min_f32_e32 v55, v56, v55
	v_max_f32_e32 v56, v32, v54
	v_min_f32_e32 v32, v32, v54
	v_max_f32_e32 v15, v10, v11
	v_min_f32_e32 v10, v10, v11
	v_min_f32_e32 v11, v40, v38
	v_max_f32_e32 v41, v4, v13
	v_max_f32_e32 v54, v25, v53
	v_min_f32_e32 v25, v25, v53
	v_min_f32_e32 v53, v58, v57
	v_max_f32_e32 v59, v30, v32
	v_min_f32_e32 v4, v4, v13
	v_max_f32_e32 v13, v41, v11
	v_min_f32_e32 v11, v41, v11
	v_max_f32_e32 v41, v8, v34
	v_min_f32_e32 v8, v8, v34
	v_max_f32_e32 v34, v3, v10
	v_min_f32_e32 v30, v30, v32
	v_max_f32_e32 v32, v59, v53
	v_min_f32_e32 v53, v59, v53
	v_max_f32_e32 v59, v50, v55
	v_min_f32_e32 v50, v50, v55
	v_max_f32_e32 v55, v24, v25
	v_min_f32_e32 v3, v3, v10
	v_max_f32_e32 v10, v34, v8
	v_min_f32_e32 v8, v34, v8
	v_min_f32_e32 v24, v24, v25
	v_max_f32_e32 v25, v55, v50
	v_min_f32_e32 v50, v55, v50
	v_max_f32_e32 v34, v41, v13
	v_min_f32_e32 v13, v41, v13
	v_max_f32_e32 v41, v10, v11
	v_min_f32_e32 v10, v10, v11
	v_max_f32_e32 v11, v8, v4
	v_min_f32_e32 v4, v8, v4
	v_max_f32_e32 v8, v7, v19
	v_min_f32_e32 v7, v7, v19
	v_max_f32_e32 v19, v6, v15
	v_max_f32_e32 v55, v59, v32
	v_min_f32_e32 v32, v59, v32
	v_max_f32_e32 v59, v25, v53
	v_min_f32_e32 v25, v25, v53
	v_max_f32_e32 v53, v50, v30
	v_min_f32_e32 v30, v50, v30
	v_max_f32_e32 v50, v49, v51
	v_min_f32_e32 v49, v49, v51
	v_max_f32_e32 v51, v48, v54
	v_min_f32_e32 v6, v6, v15
	v_max_f32_e32 v15, v19, v7
	v_min_f32_e32 v7, v19, v7
	v_max_f32_e32 v19, v9, v36
	v_min_f32_e32 v9, v9, v36
	v_max_f32_e32 v36, v2, v5
	v_min_f32_e32 v48, v48, v54
	v_max_f32_e32 v54, v51, v49
	v_min_f32_e32 v49, v51, v49
	v_max_f32_e32 v51, v52, v56
	v_min_f32_e32 v52, v52, v56
	v_max_f32_e32 v56, v23, v21
	v_min_f32_e32 v2, v2, v5
	v_max_f32_e32 v5, v36, v9
	v_min_f32_e32 v9, v36, v9
	v_max_f32_e32 v36, v19, v15
	v_min_f32_e32 v21, v23, v21
	v_max_f32_e32 v23, v56, v52
	v_min_f32_e32 v52, v56, v52
	v_and_b32_e32 v20, 0xffffff80, v72
	v_min_f32_e32 v15, v19, v15
	v_max_f32_e32 v19, v5, v7
	v_min_f32_e32 v5, v5, v7
	v_max_f32_e32 v7, v9, v6
	v_min_f32_e32 v6, v9, v6
	v_min_f32_e32 v9, v8, v34
	v_min_f32_e32 v42, v36, v13
	v_max_f32_e32 v56, v51, v54
	v_min_f32_e32 v51, v51, v54
	v_max_f32_e32 v54, v23, v49
	v_min_f32_e32 v23, v23, v49
	v_max_f32_e32 v49, v52, v48
	v_min_f32_e32 v48, v52, v48
	v_and_b32_e32 v39, 0xffffff80, v65
	v_min_f32_e32 v65, v48, v24
	v_max3_f32 v9, v9, v48, v24
	v_max3_f32 v24, v42, v49, v30
	v_add_f32_e32 v27, v27, v28
	v_add_f32_e32 v28, v20, v17
	v_add_f32_e32 v42, v20, v18
	v_add_f32_e32 v20, v20, v26
	v_and_b32_e32 v22, 0xffffff80, v73
	v_and_or_b32 v27, v27, s3, 51
	v_and_or_b32 v28, v28, s3, 64
	v_and_b32_e32 v42, 0xffffff00, v42
	v_and_b32_e32 v20, 0xffffff00, v20
	v_and_b32_e32 v29, 0xffffff80, v74
	v_and_b32_e32 v31, 0xffffff80, v75
	v_and_b32_e32 v33, 0xffffff80, v70
	v_and_b32_e32 v35, 0xffffff80, v71
	v_and_b32_e32 v37, 0xffffff80, v64
;     __device__ __forceinline__ void fused(f32x4 (&acc)[2][2][4][2], const Unit& u, int wr, int wc, int fr, int fq, PG8_LAS unsigned char* lds, int wid, int lane) const {
;     ...
;             { float cv[16]; cv[0] = __uint_as_float((__float_as_uint(v0[1] + v1[0]) & ~255u) | 16u); cv[1] = __uint_as_float((__float_as_uint(v0[1] + v1[1]) & ~255u) | 17u); cv[2] = __uint_as_float((__float_as_uint(v0[1] + v1[2]) & ~255u) | 18u); cv[3] = __uint_as_float((__float_as_uint(v0[1] + v1[3]) & ~255u) | 19u); cv[4] = __uint_as_float((__float_as_uint(v0[1] + v1[4]) & ~255u) | 20u); cv[5] = __uint_as_float((__float_as_uint(v0[1] + v1[5]) & ~255u) | 21u); cv[6] = __uint_as_float((__float_as_uint(v0[1] + v1[6]) & ~255u) | 22u); cv[7] = __uint_as_float((__float_as_uint(v0[1] + v1[7]) & ~255u) | 23u); cv[8] = __uint_as_float((__float_as_uint(v0[2] + v1[0]) & ~255u) | 32u); cv[9] = __uint_as_float((__float_as_uint(v0[2] + v1[1]) & ~255u) | 33u); cv[10] = __uint_as_float((__float_as_uint(v0[2] + v1[2]) & ~255u) | 34u); cv[11] = __uint_as_float((__float_as_uint(v0[2] + v1[3]) & ~255u) | 35u); cv[12] = __uint_as_float((__float_as_uint(v0[2] + v1[4]) & ~255u) | 36u); cv[13] = __uint_as_float((__float_as_uint(v0[3] + v1[0]) & ~255u) | 48u); cv[14] = __uint_as_float((__float_as_uint(v0[3] + v1[1]) & ~255u) | 49u); cv[15] = __uint_as_float((__float_as_uint(v0[3] + v1[2]) & ~255u) | 50u); sort16_desc(cv); merge_top16(best, cv); }
	v_min_f32_e32 v43, v15, v41
	v_min_f32_e32 v44, v19, v10
	v_min_f32_e32 v62, v54, v25
	v_or_b32_e32 v42, 0x41, v42
	v_or_b32_e32 v20, 0x42, v20
	v_add_f32_e32 v26, v22, v17
	v_add_f32_e32 v22, v22, v18
	v_min_f32_e32 v63, v23, v53
	v_max3_f32 v23, v43, v23, v53
	v_max3_f32 v10, v19, v10, v62
	v_max3_f32 v19, v44, v54, v25
	v_and_b32_e32 v26, 0xffffff00, v26
	v_and_b32_e32 v22, 0xffffff00, v22
	v_add_f32_e32 v43, v29, v17
	v_add_f32_e32 v29, v29, v18
	v_add_f32_e32 v44, v31, v17
	v_add_f32_e32 v18, v31, v18
	v_add_f32_e32 v31, v33, v17
	v_add_f32_e32 v33, v35, v17
	v_add_f32_e32 v35, v37, v17
	v_add_f32_e32 v37, v39, v17
	v_max_f32_e32 v39, v27, v28
	v_min_f32_e32 v27, v27, v28
	v_max_f32_e32 v28, v42, v42
	v_or_b32_e32 v26, 0x50, v26
	v_or_b32_e32 v22, 0x51, v22
	v_and_b32_e32 v43, 0xffffff00, v43
	v_and_b32_e32 v29, 0xffffff00, v29
	v_max_f32_e32 v42, v28, v20
	v_min_f32_e32 v20, v28, v20
	v_or_b32_e32 v43, 0x60, v43
	v_or_b32_e32 v29, 0x61, v29
	v_max_f32_e32 v28, v39, v42
	v_min_f32_e32 v39, v39, v42
	v_max_f32_e32 v42, v27, v20
	v_min_f32_e32 v20, v27, v20
	v_max_f32_e32 v27, v42, v39
	v_min_f32_e32 v39, v42, v39
	v_max_f32_e32 v42, v26, v22
	v_min_f32_e32 v22, v26, v22
	v_max_f32_e32 v26, v29, v29
	v_max_f32_e32 v29, v43, v43
	v_max_f32_e32 v43, v29, v26
	v_min_f32_e32 v26, v29, v26
	v_max_f32_e32 v29, v42, v43
	v_min_f32_e32 v42, v42, v43
	v_max_f32_e32 v43, v22, v26
	v_and_b32_e32 v12, 0xffffff80, v68
	v_and_b32_e32 v14, 0xffffff80, v69
	v_min_f32_e32 v22, v22, v26
	v_max_f32_e32 v26, v43, v42
	v_min_f32_e32 v42, v43, v42
	v_add_f32_e32 v12, v12, v17
	v_add_f32_e32 v14, v14, v17
	v_max_f32_e32 v43, v28, v29
	v_min_f32_e32 v28, v28, v29
	v_max_f32_e32 v29, v39, v42
	v_and_b32_e32 v44, 0xffffff00, v44
	v_and_b32_e32 v18, 0xffffff00, v18
	v_and_b32_e32 v12, 0xffffff00, v12
	v_and_b32_e32 v14, 0xffffff00, v14
	v_min_f32_e32 v39, v39, v42
	v_max_f32_e32 v42, v29, v28
	v_min_f32_e32 v28, v29, v28
	v_max_f32_e32 v29, v27, v26
	v_min_f32_e32 v26, v27, v26
	v_max_f32_e32 v27, v20, v22
	v_or_b32_e32 v44, 0x70, v44
	v_or_b32_e32 v18, 0x71, v18
	v_or_b32_e32 v12, 0x80, v12
	v_or_b32_e32 v14, 0x90, v14
	v_min_f32_e32 v20, v20, v22
	v_max_f32_e32 v22, v27, v26
	v_min_f32_e32 v26, v27, v26
	v_and_b32_e32 v31, 0xffffff00, v31
	v_and_b32_e32 v33, 0xffffff00, v33
	v_max_f32_e32 v27, v29, v42
	v_min_f32_e32 v29, v29, v42
	v_max_f32_e32 v42, v22, v28
	v_min_f32_e32 v22, v22, v28
	v_max_f32_e32 v28, v26, v39
	v_min_f32_e32 v26, v26, v39
	v_max_f32_e32 v39, v44, v44
	v_or_b32_e32 v31, 0xa0, v31
	v_or_b32_e32 v33, 0xb0, v33
	v_and_b32_e32 v35, 0xffffff00, v35
	v_and_b32_e32 v37, 0xffffff00, v37
	v_max_f32_e32 v44, v39, v18
	v_min_f32_e32 v18, v39, v18
	v_max_f32_e32 v39, v12, v14
	v_min_f32_e32 v12, v12, v14
	v_or_b32_e32 v35, 0xc0, v35
	v_or_b32_e32 v37, 0xd0, v37
	v_max_f32_e32 v14, v44, v39
	v_min_f32_e32 v39, v44, v39
	v_max_f32_e32 v44, v18, v12
	v_min_f32_e32 v12, v18, v12
	v_max_f32_e32 v18, v44, v39
	v_min_f32_e32 v39, v44, v39
	v_max_f32_e32 v44, v31, v33
	v_min_f32_e32 v31, v31, v33
	v_max_f32_e32 v33, v37, v37
	v_max_f32_e32 v37, v35, v33
	v_min_f32_e32 v33, v35, v33
	v_max_f32_e32 v35, v44, v37
	v_min_f32_e32 v37, v44, v37
	v_max_f32_e32 v44, v31, v33
	v_min_f32_e32 v31, v31, v33
	v_max_f32_e32 v33, v44, v37
	v_min_f32_e32 v37, v44, v37
	v_max_f32_e32 v44, v14, v35
	v_min_f32_e32 v14, v14, v35
	v_max_f32_e32 v35, v39, v37
	v_min_f32_e32 v37, v39, v37
	v_max_f32_e32 v39, v35, v14
	v_min_f32_e32 v14, v35, v14
	v_max_f32_e32 v35, v18, v33
	v_min_f32_e32 v18, v18, v33
	v_max_f32_e32 v33, v12, v31
	v_min_f32_e32 v12, v12, v31
	v_max_f32_e32 v31, v33, v18
	v_min_f32_e32 v45, v5, v11
	v_min_f32_e32 v61, v51, v59
	v_min_f32_e32 v18, v33, v18
	v_max_f32_e32 v33, v35, v39
	v_min_f32_e32 v35, v35, v39
	v_max_f32_e32 v39, v31, v14
	v_min_f32_e32 v14, v31, v14
	v_max3_f32 v5, v5, v11, v61
	v_max3_f32 v11, v45, v51, v59
	v_max_f32_e32 v31, v18, v37
	v_min_f32_e32 v18, v18, v37
	v_min_f32_e32 v37, v43, v44
	v_max_f32_e32 v45, v22, v14
	v_min_f32_e32 v14, v22, v14
	v_max_f32_e32 v22, v45, v37
	v_min_f32_e32 v37, v45, v37
	v_max_f32_e32 v45, v29, v35
	v_min_f32_e32 v29, v29, v35
	v_max_f32_e32 v35, v26, v18
	v_min_f32_e32 v46, v7, v4
	v_min_f32_e32 v47, v6, v3
	v_min_f32_e32 v52, v50, v55
	v_min_f32_e32 v60, v56, v32
	v_min_f32_e32 v64, v49, v30
	v_min_f32_e32 v18, v26, v18
	v_max_f32_e32 v26, v35, v29
	v_min_f32_e32 v29, v35, v29
	v_max3_f32 v21, v40, v38, v21
	v_max3_f32 v8, v8, v34, v65
	v_max3_f32 v13, v36, v13, v64
	v_max3_f32 v15, v15, v41, v63
	v_max3_f32 v4, v7, v4, v60
	v_max3_f32 v7, v46, v56, v32
	v_max3_f32 v3, v6, v3, v52
	v_max3_f32 v6, v47, v50, v55
	v_max3_f32 v2, v2, v58, v57
	v_max_f32_e32 v35, v45, v22
	v_min_f32_e32 v22, v45, v22
	v_max_f32_e32 v45, v26, v37
	v_min_f32_e32 v26, v26, v37
	v_max_f32_e32 v37, v29, v14
	v_min_f32_e32 v14, v29, v14
	v_max_f32_e32 v29, v27, v33
	v_min_f32_e32 v27, v27, v33
	v_max_f32_e32 v33, v28, v31
	v_max_f32_e32 v25, v21, v19
	v_min_f32_e32 v19, v21, v19
	v_max_f32_e32 v21, v8, v5
	v_min_f32_e32 v5, v8, v5
	v_max_f32_e32 v8, v9, v11
	v_min_f32_e32 v9, v9, v11
	v_max_f32_e32 v11, v13, v4
	v_min_f32_e32 v4, v13, v4
	v_max_f32_e32 v13, v24, v7
	v_min_f32_e32 v7, v24, v7
	v_max_f32_e32 v24, v15, v3
	v_min_f32_e32 v3, v15, v3
	v_max_f32_e32 v15, v23, v6
	v_min_f32_e32 v6, v23, v6
	v_max_f32_e32 v23, v10, v2
	v_min_f32_e32 v2, v10, v2
	v_min_f32_e32 v28, v28, v31
	v_max_f32_e32 v31, v33, v27
	v_min_f32_e32 v27, v33, v27
	v_max_f32_e32 v33, v42, v39
	v_min_f32_e32 v39, v42, v39
	v_max_f32_e32 v42, v20, v12
	v_max_f32_e32 v10, v25, v13
	v_min_f32_e32 v13, v25, v13
	v_max_f32_e32 v25, v21, v24
	v_min_f32_e32 v21, v21, v24
;     __device__ __forceinline__ void fused(f32x4 (&acc)[2][2][4][2], const Unit& u, int wr, int wc, int fr, int fq, PG8_LAS unsigned char* lds, int wid, int lane) const {
;     ...
;             { float cv[16]; cv[0] = __uint_as_float((__float_as_uint(v0[14] + v1[0]) & ~255u) | 224u); cv[1] = __uint_as_float((__float_as_uint(v0[15] + v1[0]) & ~255u) | 240u); cv[2] = -INFINITY; cv[3] = -INFINITY; cv[4] = -INFINITY; cv[5] = -INFINITY; cv[6] = -INFINITY; cv[7] = -INFINITY; cv[8] = -INFINITY; cv[9] = -INFINITY; cv[10] = -INFINITY; cv[11] = -INFINITY; cv[12] = -INFINITY; cv[13] = -INFINITY; cv[14] = -INFINITY; cv[15] = -INFINITY; sort16_desc(cv); merge_top16(best, cv); }
;             float sc[16], sum = 0.f;
; #pragma unroll
;             for (int q = 0; q < 16; ++q) { sc[q] = __uint_as_float(__float_as_uint(best[q]) & ~255u); }
;             const float smax = sc[0];
; #pragma unroll
;             for (int q = 0; q < 16; ++q) { sc[q] = __builtin_amdgcn_exp2f((sc[q] - smax) * 1.4426950408889634f); }
; #pragma unroll
;             for (int q = 0; q < 16; ++q) sum += sc[q];
;             const float rs = 1.0f / sum;
;             asm volatile("s_waitcnt lgkmcnt(0)" ::: "memory");
;             int ex[16];
; #pragma unroll
;             for (int q = 0; q < 16; ++q) { const unsigned cid = __float_as_uint(best[q]) & 255u; ex[q] = idxl[cid >> 4] * 128 + idxl[16 + (cid & 15u)]; }
	v_max_f32_e32 v24, v8, v15
	v_min_f32_e32 v8, v8, v15
	v_max_f32_e32 v15, v11, v23
	v_min_f32_e32 v11, v11, v23
	v_max_f32_e32 v23, v19, v7
	v_min_f32_e32 v7, v19, v7
	v_max_f32_e32 v19, v5, v3
	v_min_f32_e32 v3, v5, v3
	v_max_f32_e32 v5, v9, v6
	v_min_f32_e32 v6, v9, v6
	v_max_f32_e32 v9, v4, v2
	v_min_f32_e32 v2, v4, v2
	v_min_f32_e32 v12, v20, v12
	v_max_f32_e32 v20, v42, v39
	v_min_f32_e32 v39, v42, v39
	v_and_b32_e32 v1, 0xffffff80, v66
	v_and_b32_e32 v0, 0xffffff80, v67
	v_max_f32_e32 v4, v10, v24
	v_min_f32_e32 v10, v10, v24
	v_max_f32_e32 v24, v25, v15
	v_min_f32_e32 v15, v25, v15
	v_max_f32_e32 v25, v13, v8
	v_min_f32_e32 v8, v13, v8
	v_max_f32_e32 v13, v21, v11
	v_min_f32_e32 v11, v21, v11
	v_max_f32_e32 v21, v23, v5
	v_min_f32_e32 v5, v23, v5
	v_max_f32_e32 v23, v19, v9
	v_min_f32_e32 v9, v19, v9
	v_max_f32_e32 v19, v7, v6
	v_min_f32_e32 v6, v7, v6
	v_max_f32_e32 v7, v3, v2
	v_min_f32_e32 v2, v3, v2
	v_max_f32_e32 v42, v33, v31
	v_min_f32_e32 v31, v33, v31
	v_max_f32_e32 v33, v20, v27
	v_min_f32_e32 v20, v20, v27
	v_max_f32_e32 v27, v39, v28
	v_min_f32_e32 v28, v39, v28
	v_min_f32_e32 v3, v4, v24
	v_min_f32_e32 v30, v10, v15
	v_min_f32_e32 v32, v25, v13
	v_min_f32_e32 v34, v8, v11
	v_min_f32_e32 v36, v21, v23
	v_min_f32_e32 v38, v5, v9
	v_min_f32_e32 v40, v19, v7
	v_min_f32_e32 v41, v6, v2
	v_max_f32_e32 v39, v29, v35
	v_min_f32_e32 v29, v29, v35
	v_max_f32_e32 v35, v42, v22
	v_min_f32_e32 v22, v42, v22
	v_max_f32_e32 v42, v31, v45
	v_min_f32_e32 v31, v31, v45
	v_max_f32_e32 v45, v33, v26
	v_min_f32_e32 v26, v33, v26
	v_max_f32_e32 v33, v20, v37
	v_min_f32_e32 v20, v20, v37
	v_max_f32_e32 v37, v27, v14
	v_min_f32_e32 v14, v27, v14
	v_max_f32_e32 v27, v28, v18
	v_min_f32_e32 v18, v28, v18
	v_add_f32_e32 v1, v1, v17
	v_add_f32_e32 v0, v0, v17
	v_max3_f32 v4, v4, v24, v12
	v_max_f32_e32 v3, v3, v18
	v_max3_f32 v10, v10, v15, v27
	v_max_f32_e32 v12, v30, v14
	v_max3_f32 v13, v25, v13, v37
	v_max_f32_e32 v14, v32, v20
	v_max3_f32 v8, v8, v11, v33
	v_max_f32_e32 v11, v34, v26
	v_max3_f32 v15, v21, v23, v45
	v_max_f32_e32 v18, v36, v31
	v_max3_f32 v5, v5, v9, v42
	v_max_f32_e32 v9, v38, v22
	v_max3_f32 v7, v19, v7, v35
	v_max_f32_e32 v19, v40, v29
	v_max3_f32 v2, v6, v2, v39
	v_max3_f32 v6, v41, v43, v44
	v_and_b32_e32 v1, 0xffffff00, v1
	v_and_b32_e32 v0, 0xffffff00, v0
	v_max_f32_e32 v20, v4, v15
	v_min_f32_e32 v4, v4, v15
	v_max_f32_e32 v15, v3, v18
	v_min_f32_e32 v3, v3, v18
	v_max_f32_e32 v18, v10, v5
	v_min_f32_e32 v5, v10, v5
	v_max_f32_e32 v10, v12, v9
	v_min_f32_e32 v9, v12, v9
	v_max_f32_e32 v12, v13, v7
	v_min_f32_e32 v7, v13, v7
	v_max_f32_e32 v13, v14, v19
	v_min_f32_e32 v14, v14, v19
	v_max_f32_e32 v19, v8, v2
	v_min_f32_e32 v2, v8, v2
	v_max_f32_e32 v8, v11, v6
	v_min_f32_e32 v6, v11, v6
	v_or_b32_e32 v1, 0xe0, v1
	v_or_b32_e32 v0, 0xf0, v0
	v_max_f32_e32 v11, v20, v12
	v_min_f32_e32 v12, v20, v12
	v_max_f32_e32 v20, v15, v13
	v_min_f32_e32 v13, v15, v13
	v_max_f32_e32 v15, v18, v19
	v_min_f32_e32 v18, v18, v19
	v_max_f32_e32 v19, v10, v8
	v_min_f32_e32 v8, v10, v8
	v_max_f32_e32 v10, v4, v7
	v_min_f32_e32 v4, v4, v7
	v_max_f32_e32 v7, v3, v14
	v_min_f32_e32 v3, v3, v14
	v_max_f32_e32 v14, v5, v2
	v_min_f32_e32 v2, v5, v2
	v_max_f32_e32 v5, v9, v6
	v_min_f32_e32 v6, v9, v6
	v_max_f32_e32 v9, v11, v15
	v_min_f32_e32 v11, v11, v15
	v_max_f32_e32 v15, v20, v19
	v_min_f32_e32 v19, v20, v19
	v_max_f32_e32 v20, v12, v18
	v_min_f32_e32 v12, v12, v18
	v_max_f32_e32 v18, v13, v8
	v_min_f32_e32 v8, v13, v8
	v_max_f32_e32 v13, v10, v14
	v_min_f32_e32 v10, v10, v14
	v_max_f32_e32 v14, v7, v5
	v_min_f32_e32 v5, v7, v5
	v_max_f32_e32 v7, v4, v2
	v_min_f32_e32 v2, v4, v2
	v_max_f32_e32 v4, v3, v6
	v_min_f32_e32 v3, v3, v6
	v_max_f32_e32 v17, v1, v0
	v_min_f32_e32 v0, v1, v0
	v_min_f32_e32 v6, v9, v15
	v_min_f32_e32 v21, v11, v19
	v_min_f32_e32 v22, v20, v18
	v_min_f32_e32 v23, v12, v8
	v_min_f32_e32 v24, v13, v14
	v_min_f32_e32 v25, v10, v5
	v_min_f32_e32 v26, v7, v4
	v_min_f32_e32 v27, v2, v3
	s_mov_b32 s3, 0xff800000
	v_max_f32_e32 v0, 0xff800000, v0
	v_max3_f32 v1, v9, v15, s3
	v_max_f32_e32 v6, 0xff800000, v6
	v_max3_f32 v9, v11, v19, s3
	v_max_f32_e32 v11, 0xff800000, v21
	v_max3_f32 v15, v20, v18, s3
	v_max_f32_e32 v18, 0xff800000, v22
	v_max3_f32 v8, v12, v8, s3
	v_max_f32_e32 v12, 0xff800000, v23
	v_max3_f32 v13, v13, v14, s3
	v_max_f32_e32 v14, 0xff800000, v24
	v_max3_f32 v5, v10, v5, s3
	v_max_f32_e32 v10, 0xff800000, v25
	v_max3_f32 v4, v7, v4, s3
	v_max_f32_e32 v7, 0xff800000, v26
	v_max3_f32 v0, v2, v3, v0
	v_max3_f32 v2, v27, v17, s3
	v_max_f32_e32 v3, v1, v13
	v_min_f32_e32 v1, v1, v13
	v_max_f32_e32 v13, v6, v14
	v_min_f32_e32 v6, v6, v14
	v_max_f32_e32 v14, v9, v5
	v_min_f32_e32 v5, v9, v5
	v_max_f32_e32 v9, v11, v10
	v_min_f32_e32 v10, v11, v10
	v_max_f32_e32 v11, v15, v4
	v_min_f32_e32 v4, v15, v4
	v_max_f32_e32 v15, v18, v7
	v_max_f32_e32 v17, v8, v0
	v_min_f32_e32 v0, v8, v0
	v_max_f32_e32 v8, v12, v2
	v_min_f32_e32 v2, v12, v2
	v_max_f32_e32 v12, v3, v11
	v_min_f32_e32 v3, v3, v11
	v_max_f32_e32 v11, v13, v15
	v_min_f32_e32 v13, v13, v15
	v_max_f32_e32 v15, v14, v17
	v_min_f32_e32 v14, v14, v17
	v_max_f32_e32 v17, v9, v8
	v_min_f32_e32 v8, v9, v8
	v_max_f32_e32 v9, v1, v4
	v_min_f32_e32 v24, v1, v4
	v_max_f32_e32 v27, v5, v0
	v_min_f32_e32 v28, v5, v0
	v_max_f32_e32 v29, v10, v2
	v_min_f32_e32 v30, v10, v2
	v_max_f32_e32 v0, v12, v15
	v_min_f32_e32 v1, v12, v15
	v_max_f32_e32 v2, v11, v17
	v_min_f32_e32 v4, v11, v17
	v_min_f32_e32 v7, v18, v7
	v_max_f32_e32 v33, v0, v2
	v_min_f32_e32 v34, v0, v2
	v_min_f32_e32 v36, v1, v4
	v_max_f32_e32 v25, v6, v7
	v_min_f32_e32 v26, v6, v7
	v_max_f32_e32 v35, v1, v4
	v_lshrrev_b32_e32 v0, 2, v33
	v_lshrrev_b32_e32 v2, 2, v34
	v_lshrrev_b32_e32 v6, 2, v36
	v_max_f32_e32 v17, v3, v14
	v_min_f32_e32 v31, v3, v14
	v_and_b32_e32 v0, 60, v0
	v_and_b32_e32 v1, 15, v33
	v_and_b32_e32 v2, 60, v2
	v_and_b32_e32 v3, 15, v34
	v_lshrrev_b32_e32 v4, 2, v35
	v_and_b32_e32 v5, 15, v35
	v_and_b32_e32 v6, 60, v6
	v_and_b32_e32 v7, 15, v36
	s_waitcnt lgkmcnt(0)
; #define RT_PK(q_) (ex[q_] | (int)((__float_as_uint(usc[ex[q_]]) >> 23) << 14))
;     __device__ __forceinline__ void fused(f32x4 (&acc)[2][2][4][2], const Unit& u, int wr, int wc, int fr, int fq, PG8_LAS unsigned char* lds, int wid, int lane) const {
;     ...
;             for (int q = 0; q < 16; ++q) { sc[q] = __uint_as_float(__float_as_uint(best[q]) & ~255u); }
;             const float smax = sc[0];
; #pragma unroll
;             for (int q = 0; q < 16; ++q) { sc[q] = __builtin_amdgcn_exp2f((sc[q] - smax) * 1.4426950408889634f); }
; #pragma unroll
;             for (int q = 0; q < 16; ++q) sum += sc[q];
;             const float rs = 1.0f / sum;
;             asm volatile("s_waitcnt lgkmcnt(0)" ::: "memory");
;             int ex[16];
; #pragma unroll
;             for (int q = 0; q < 16; ++q) { const unsigned cid = __float_as_uint(best[q]) & 255u; ex[q] = idxl[cid >> 4] * 128 + idxl[16 + (cid & 15u)]; }
;             const size_t o = ((size_t)u.pn * 16384 + (size_t)(u.pm * BM + row)) * 16;
;             typedef int i32x4 __attribute__((ext_vector_type(4)));
; #pragma unroll
;             for (int i = 0; i < 4; ++i) {
;     ...
;                 *(i32x4*)(eidx + o + 4 * i) = (i32x4){RT_PK(4 * i), RT_PK(4 * i + 1), RT_PK(4 * i + 2), RT_PK(4 * i + 3)};
;                 *(f32x4*)(egate + o + 4 * i) = (f32x4){sc[4 * i] * rs * vsc[ex[4 * i]], sc[4 * i + 1] * rs * vsc[ex[4 * i + 1]], sc[4 * i + 2] * rs * vsc[ex[4 * i + 2]], sc[4 * i + 3] * rs * vsc[ex[4 * i + 3]]};
	v_add_u32_e32 v0, v16, v0
	v_lshl_add_u32 v1, v1, 2, v16
	v_add_u32_e32 v2, v16, v2
	v_lshl_add_u32 v3, v3, 2, v16
	v_and_b32_e32 v4, 60, v4
	v_lshl_add_u32 v5, v5, 2, v16
	v_add_u32_e32 v6, v16, v6
	v_lshl_add_u32 v7, v7, 2, v16
	v_add_u32_e32 v4, v16, v4
	ds_read_b32 v0, v0
	ds_read_b32 v1, v1 offset:64
	ds_read_b32 v2, v2
	ds_read_b32 v3, v3 offset:64
	ds_read_b32 v10, v4
	ds_read_b32 v5, v5 offset:64
	ds_read_b32 v6, v6
	ds_read_b32 v7, v7 offset:64
	s_waitcnt lgkmcnt(0)
	v_lshl_add_u32 v0, v0, 7, v1
	v_ashrrev_i32_e32 v1, 31, v0
	v_lshl_add_u32 v4, v2, 7, v3
	v_lshlrev_b64 v[14:15], 2, v[0:1]
	v_lshl_add_u32 v10, v10, 7, v5
	v_lshl_add_u32 v12, v6, 7, v7
	v_lshl_add_u64 v[2:3], s[8:9], 0, v[14:15]
	v_ashrrev_i32_e32 v5, 31, v4
	v_max_f32_e32 v32, v13, v8
	v_min_f32_e32 v8, v13, v8
	global_load_dword v1, v[2:3], off
	v_lshlrev_b64 v[18:19], 2, v[4:5]
	v_ashrrev_i32_e32 v11, 31, v10
	v_ashrrev_i32_e32 v13, 31, v12
	v_lshl_add_u64 v[2:3], s[8:9], 0, v[18:19]
	v_lshlrev_b64 v[20:21], 2, v[10:11]
	v_lshlrev_b64 v[22:23], 2, v[12:13]
	v_lshl_add_u64 v[6:7], s[8:9], 0, v[20:21]
	global_load_dword v5, v[2:3], off
	global_load_dword v11, v[6:7], off
	v_lshl_add_u64 v[2:3], s[8:9], 0, v[22:23]
	global_load_dword v13, v[2:3], off
	v_min_f32_e32 v2, v9, v27
	v_min_f32_e32 v6, v25, v29
	v_max_f32_e32 v43, v2, v6
	v_min_f32_e32 v44, v2, v6
	v_and_b32_e32 v2, 0xffffff00, v34
	v_and_b32_e32 v51, 0xffffff00, v33
	v_max_f32_e32 v37, v9, v27
	v_max_f32_e32 v3, v25, v29
	v_sub_f32_e32 v2, v2, v51
	v_min_f32_e32 v9, v24, v28
	v_min_f32_e32 v25, v26, v30
	v_max_f32_e32 v41, v37, v3
	v_min_f32_e32 v42, v37, v3
	v_and_b32_e32 v3, 0xffffff00, v35
	v_mul_f32_e32 v2, 0x3fb8aa3b, v2
	v_max_f32_e32 v47, v9, v25
	v_min_f32_e32 v48, v9, v25
	v_exp_f32_e32 v25, v2
	v_sub_f32_e32 v2, v3, v51
	v_and_b32_e32 v6, 0xffffff00, v36
	v_mul_f32_e32 v2, 0x3fb8aa3b, v2
	v_max_f32_e32 v7, v24, v28
	v_max_f32_e32 v24, v26, v30
	v_max_f32_e32 v38, v17, v32
	v_exp_f32_e32 v26, v2
	v_sub_f32_e32 v2, v6, v51
	v_max_f32_e32 v45, v7, v24
	v_min_f32_e32 v46, v7, v24
	v_and_b32_e32 v7, 0xffffff00, v38
	v_mul_f32_e32 v2, 0x3fb8aa3b, v2
	v_min_f32_e32 v17, v17, v32
	v_exp_f32_e32 v27, v2
	v_sub_f32_e32 v2, v7, v51
	v_max_f32_e32 v39, v31, v8
	v_min_f32_e32 v40, v31, v8
	v_lshl_add_u64 v[168:169], s[6:7], 0, v[14:15]
	global_load_dword v194, v[168:169], off
	v_lshl_add_u64 v[168:169], s[6:7], 0, v[18:19]
	global_load_dword v195, v[168:169], off
	v_lshl_add_u64 v[168:169], s[6:7], 0, v[20:21]
	global_load_dword v196, v[168:169], off
	v_lshl_add_u64 v[168:169], s[6:7], 0, v[22:23]
	global_load_dword v197, v[168:169], off
	v_lshrrev_b32_e32 v140, 2, v38
	v_and_b32_e32 v141, 15, v38
	v_and_b32_e32 v140, 60, v140
	v_lshl_add_u32 v141, v141, 2, v16
	v_add_u32_e32 v140, v16, v140
	ds_read_b32 v140, v140
	ds_read_b32 v141, v141 offset:64
	v_lshrrev_b32_e32 v142, 2, v17
	v_and_b32_e32 v143, 15, v17
	v_and_b32_e32 v142, 60, v142
	v_lshl_add_u32 v143, v143, 2, v16
	v_add_u32_e32 v142, v16, v142
	ds_read_b32 v142, v142
	ds_read_b32 v143, v143 offset:64
	v_lshrrev_b32_e32 v144, 2, v39
	v_and_b32_e32 v145, 15, v39
	v_and_b32_e32 v144, 60, v144
	v_lshl_add_u32 v145, v145, 2, v16
	v_add_u32_e32 v144, v16, v144
	ds_read_b32 v144, v144
	ds_read_b32 v145, v145 offset:64
	v_lshrrev_b32_e32 v146, 2, v40
	v_and_b32_e32 v147, 15, v40
	v_and_b32_e32 v146, 60, v146
	v_lshl_add_u32 v147, v147, 2, v16
	v_add_u32_e32 v146, v16, v146
	ds_read_b32 v146, v146
	ds_read_b32 v147, v147 offset:64
	v_lshrrev_b32_e32 v148, 2, v41
	v_and_b32_e32 v149, 15, v41
	v_and_b32_e32 v148, 60, v148
	v_lshl_add_u32 v149, v149, 2, v16
	v_add_u32_e32 v148, v16, v148
	ds_read_b32 v148, v148
	ds_read_b32 v149, v149 offset:64
	v_lshrrev_b32_e32 v150, 2, v42
	v_and_b32_e32 v151, 15, v42
	v_and_b32_e32 v150, 60, v150
	v_lshl_add_u32 v151, v151, 2, v16
	v_add_u32_e32 v150, v16, v150
	ds_read_b32 v150, v150
	ds_read_b32 v151, v151 offset:64
	v_lshrrev_b32_e32 v152, 2, v43
	v_and_b32_e32 v153, 15, v43
	v_and_b32_e32 v152, 60, v152
	v_lshl_add_u32 v153, v153, 2, v16
	v_add_u32_e32 v152, v16, v152
	ds_read_b32 v152, v152
	ds_read_b32 v153, v153 offset:64
	v_lshrrev_b32_e32 v154, 2, v44
	v_and_b32_e32 v155, 15, v44
	v_and_b32_e32 v154, 60, v154
	v_lshl_add_u32 v155, v155, 2, v16
	v_add_u32_e32 v154, v16, v154
	ds_read_b32 v154, v154
	ds_read_b32 v155, v155 offset:64
	v_lshrrev_b32_e32 v156, 2, v45
	v_and_b32_e32 v157, 15, v45
	v_and_b32_e32 v156, 60, v156
	v_lshl_add_u32 v157, v157, 2, v16
	v_add_u32_e32 v156, v16, v156
	ds_read_b32 v156, v156
	ds_read_b32 v157, v157 offset:64
	v_lshrrev_b32_e32 v158, 2, v46
	v_and_b32_e32 v159, 15, v46
	v_and_b32_e32 v158, 60, v158
	v_lshl_add_u32 v159, v159, 2, v16
	v_add_u32_e32 v158, v16, v158
	ds_read_b32 v158, v158
	ds_read_b32 v159, v159 offset:64
	v_lshrrev_b32_e32 v160, 2, v47
	v_and_b32_e32 v161, 15, v47
	v_and_b32_e32 v160, 60, v160
	v_lshl_add_u32 v161, v161, 2, v16
	v_add_u32_e32 v160, v16, v160
	ds_read_b32 v160, v160
	ds_read_b32 v161, v161 offset:64
	v_lshrrev_b32_e32 v162, 2, v48
	v_and_b32_e32 v163, 15, v48
	v_and_b32_e32 v162, 60, v162
	v_lshl_add_u32 v163, v163, 2, v16
	v_add_u32_e32 v162, v16, v162
	ds_read_b32 v162, v162
	ds_read_b32 v163, v163 offset:64
	s_waitcnt lgkmcnt(0)
; #define RT_PK(q_) (ex[q_] | (int)((__float_as_uint(usc[ex[q_]]) >> 23) << 14))
;     __device__ __forceinline__ void fused(f32x4 (&acc)[2][2][4][2], const Unit& u, int wr, int wc, int fr, int fq, PG8_LAS unsigned char* lds, int wid, int lane) const {
;     ...
;             for (int q = 0; q < 16; ++q) { const unsigned cid = __float_as_uint(best[q]) & 255u; ex[q] = idxl[cid >> 4] * 128 + idxl[16 + (cid & 15u)]; }
;             const size_t o = ((size_t)u.pn * 16384 + (size_t)(u.pm * BM + row)) * 16;
;             typedef int i32x4 __attribute__((ext_vector_type(4)));
; #pragma unroll
;             for (int i = 0; i < 4; ++i) {
;     ...
;                 *(i32x4*)(eidx + o + 4 * i) = (i32x4){RT_PK(4 * i), RT_PK(4 * i + 1), RT_PK(4 * i + 2), RT_PK(4 * i + 3)};
;                 *(f32x4*)(egate + o + 4 * i) = (f32x4){sc[4 * i] * rs * vsc[ex[4 * i]], sc[4 * i + 1] * rs * vsc[ex[4 * i + 1]], sc[4 * i + 2] * rs * vsc[ex[4 * i + 2]], sc[4 * i + 3] * rs * vsc[ex[4 * i + 3]]};
	v_lshl_add_u32 v164, v140, 7, v141
	v_ashrrev_i32_e32 v165, 31, v164
	v_lshlrev_b64 v[166:167], 2, v[164:165]
	v_lshl_add_u64 v[168:169], s[8:9], 0, v[166:167]
	global_load_dword v170, v[168:169], off
	v_lshl_add_u64 v[168:169], s[6:7], 0, v[166:167]
	global_load_dword v182, v[168:169], off
	v_lshl_add_u32 v164, v142, 7, v143
	v_ashrrev_i32_e32 v165, 31, v164
	v_lshlrev_b64 v[166:167], 2, v[164:165]
	v_lshl_add_u64 v[168:169], s[8:9], 0, v[166:167]
	global_load_dword v171, v[168:169], off
	v_lshl_add_u64 v[168:169], s[6:7], 0, v[166:167]
	global_load_dword v183, v[168:169], off
	v_lshl_add_u32 v164, v144, 7, v145
	v_ashrrev_i32_e32 v165, 31, v164
	v_lshlrev_b64 v[166:167], 2, v[164:165]
	v_lshl_add_u64 v[168:169], s[8:9], 0, v[166:167]
	global_load_dword v172, v[168:169], off
	v_lshl_add_u64 v[168:169], s[6:7], 0, v[166:167]
	global_load_dword v184, v[168:169], off
	v_lshl_add_u32 v164, v146, 7, v147
	v_ashrrev_i32_e32 v165, 31, v164
	v_lshlrev_b64 v[166:167], 2, v[164:165]
	v_lshl_add_u64 v[168:169], s[8:9], 0, v[166:167]
	global_load_dword v173, v[168:169], off
	v_lshl_add_u64 v[168:169], s[6:7], 0, v[166:167]
	global_load_dword v185, v[168:169], off
	v_lshl_add_u32 v164, v148, 7, v149
	v_ashrrev_i32_e32 v165, 31, v164
	v_lshlrev_b64 v[166:167], 2, v[164:165]
	v_lshl_add_u64 v[168:169], s[8:9], 0, v[166:167]
	global_load_dword v174, v[168:169], off
	v_lshl_add_u64 v[168:169], s[6:7], 0, v[166:167]
	global_load_dword v186, v[168:169], off
	v_lshl_add_u32 v164, v150, 7, v151
	v_ashrrev_i32_e32 v165, 31, v164
	v_lshlrev_b64 v[166:167], 2, v[164:165]
	v_lshl_add_u64 v[168:169], s[8:9], 0, v[166:167]
	global_load_dword v175, v[168:169], off
	v_lshl_add_u64 v[168:169], s[6:7], 0, v[166:167]
	global_load_dword v187, v[168:169], off
	v_lshl_add_u32 v164, v152, 7, v153
	v_ashrrev_i32_e32 v165, 31, v164
	v_lshlrev_b64 v[166:167], 2, v[164:165]
	v_lshl_add_u64 v[168:169], s[8:9], 0, v[166:167]
	global_load_dword v176, v[168:169], off
	v_lshl_add_u64 v[168:169], s[6:7], 0, v[166:167]
	global_load_dword v188, v[168:169], off
	v_lshl_add_u32 v164, v154, 7, v155
	v_ashrrev_i32_e32 v165, 31, v164
	v_lshlrev_b64 v[166:167], 2, v[164:165]
	v_lshl_add_u64 v[168:169], s[8:9], 0, v[166:167]
	global_load_dword v177, v[168:169], off
	v_lshl_add_u64 v[168:169], s[6:7], 0, v[166:167]
	global_load_dword v189, v[168:169], off
	v_lshl_add_u32 v164, v156, 7, v157
	v_ashrrev_i32_e32 v165, 31, v164
	v_lshlrev_b64 v[166:167], 2, v[164:165]
	v_lshl_add_u64 v[168:169], s[8:9], 0, v[166:167]
	global_load_dword v178, v[168:169], off
	v_lshl_add_u64 v[168:169], s[6:7], 0, v[166:167]
	global_load_dword v190, v[168:169], off
	v_lshl_add_u32 v164, v158, 7, v159
	v_ashrrev_i32_e32 v165, 31, v164
	v_lshlrev_b64 v[166:167], 2, v[164:165]
	v_lshl_add_u64 v[168:169], s[8:9], 0, v[166:167]
	global_load_dword v179, v[168:169], off
	v_lshl_add_u64 v[168:169], s[6:7], 0, v[166:167]
	global_load_dword v191, v[168:169], off
	v_lshl_add_u32 v164, v160, 7, v161
	v_ashrrev_i32_e32 v165, 31, v164
	v_lshlrev_b64 v[166:167], 2, v[164:165]
	v_lshl_add_u64 v[168:169], s[8:9], 0, v[166:167]
	global_load_dword v180, v[168:169], off
	v_lshl_add_u64 v[168:169], s[6:7], 0, v[166:167]
	global_load_dword v192, v[168:169], off
	v_lshl_add_u32 v164, v162, 7, v163
	v_ashrrev_i32_e32 v165, 31, v164
	v_lshlrev_b64 v[166:167], 2, v[164:165]
	v_lshl_add_u64 v[168:169], s[8:9], 0, v[166:167]
	global_load_dword v181, v[168:169], off
	v_lshl_add_u64 v[168:169], s[6:7], 0, v[166:167]
	global_load_dword v193, v[168:169], off
	v_and_b32_e32 v8, 0xffffff00, v17
	v_mul_f32_e32 v2, 0x3fb8aa3b, v2
	v_exp_f32_e32 v28, v2
	v_sub_f32_e32 v2, v8, v51
	v_and_b32_e32 v9, 0xffffff00, v39
	v_mul_f32_e32 v2, 0x3fb8aa3b, v2
	v_exp_f32_e32 v29, v2
	v_sub_f32_e32 v2, v9, v51
	v_and_b32_e32 v31, 0xffffff00, v40
	v_mul_f32_e32 v2, 0x3fb8aa3b, v2
	v_exp_f32_e32 v30, v2
	v_sub_f32_e32 v2, v31, v51
	v_and_b32_e32 v32, 0xffffff00, v41
	v_mul_f32_e32 v2, 0x3fb8aa3b, v2
	v_exp_f32_e32 v31, v2
	v_sub_f32_e32 v2, v32, v51
	v_and_b32_e32 v34, 0xffffff00, v42
	v_mul_f32_e32 v2, 0x3fb8aa3b, v2
	v_exp_f32_e32 v6, v2
	v_sub_f32_e32 v2, v34, v51
	v_and_b32_e32 v35, 0xffffff00, v43
	v_mul_f32_e32 v2, 0x3fb8aa3b, v2
	v_exp_f32_e32 v7, v2
	v_sub_f32_e32 v2, v35, v51
	v_mul_f32_e32 v2, 0x3fb8aa3b, v2
	v_exp_f32_e32 v8, v2
	v_lshl_or_b32 v2, s18, 8, v128
	v_ashrrev_i32_e32 v3, 31, v2
	s_lshl_b64 s[4:5], s[16:17], 18
	s_mov_b32 s3, 0x7fc000
	v_lshl_add_u64 v[32:33], v[2:3], 4, s[4:5]
	v_sub_f32_e32 v24, v51, v51
	v_mul_f32_e32 v24, 0x3fb8aa3b, v24
	v_exp_f32_e32 v24, v24
	s_waitcnt vmcnt(28)
; #define RT_PK(q_) (ex[q_] | (int)((__float_as_uint(usc[ex[q_]]) >> 23) << 14))
;     __device__ __forceinline__ void fused(f32x4 (&acc)[2][2][4][2], const Unit& u, int wr, int wc, int fr, int fq, PG8_LAS unsigned char* lds, int wid, int lane) const {
;     ...
;             for (int q = 0; q < 16; ++q) { sc[q] = __builtin_amdgcn_exp2f((sc[q] - smax) * 1.4426950408889634f); }
; #pragma unroll
;             for (int q = 0; q < 16; ++q) sum += sc[q];
;             const float rs = 1.0f / sum;
;             asm volatile("s_waitcnt lgkmcnt(0)" ::: "memory");
;             int ex[16];
; #pragma unroll
;             for (int q = 0; q < 16; ++q) { const unsigned cid = __float_as_uint(best[q]) & 255u; ex[q] = idxl[cid >> 4] * 128 + idxl[16 + (cid & 15u)]; }
;             const size_t o = ((size_t)u.pn * 16384 + (size_t)(u.pm * BM + row)) * 16;
;             typedef int i32x4 __attribute__((ext_vector_type(4)));
; #pragma unroll
;             for (int i = 0; i < 4; ++i) {
;     ...
;                 *(i32x4*)(eidx + o + 4 * i) = (i32x4){RT_PK(4 * i), RT_PK(4 * i + 1), RT_PK(4 * i + 2), RT_PK(4 * i + 3)};
;                 *(f32x4*)(egate + o + 4 * i) = (f32x4){sc[4 * i] * rs * vsc[ex[4 * i]], sc[4 * i + 1] * rs * vsc[ex[4 * i + 1]], sc[4 * i + 2] * rs * vsc[ex[4 * i + 2]], sc[4 * i + 3] * rs * vsc[ex[4 * i + 3]]};
	v_lshrrev_b32_e32 v1, 9, v1
	v_and_or_b32 v2, v1, s3, v0
	v_and_b32_e32 v36, 0xffffff00, v44
	v_and_b32_e32 v37, 0xffffff00, v45
	v_and_b32_e32 v49, 0xffffff00, v46
	v_and_b32_e32 v50, 0xffffff00, v47
	v_and_b32_e32 v52, 0xffffff00, v48
	v_lshrrev_b32_e32 v0, 9, v5
	v_and_or_b32 v3, v0, s3, v4
	v_lshrrev_b32_e32 v0, 9, v11
	v_and_or_b32 v4, v0, s3, v10
	v_lshrrev_b32_e32 v0, 9, v13
	v_and_or_b32 v5, v0, s3, v12
	v_lshlrev_b64 v[12:13], 2, v[32:33]
	v_lshl_add_u64 v[0:1], s[12:13], 0, v[12:13]
	global_store_dwordx4 v[0:1], v[2:5], off
	v_lshrrev_b32_e32 v32, 2, v40
	v_add_f32_e32 v10, 0, v24
	v_add_f32_e32 v10, v25, v10
	v_add_f32_e32 v10, v26, v10
	v_add_f32_e32 v10, v27, v10
	v_sub_f32_e32 v2, v36, v51
	v_add_f32_e32 v10, v28, v10
	v_mul_f32_e32 v2, 0x3fb8aa3b, v2
	v_add_f32_e32 v10, v29, v10
	v_exp_f32_e32 v9, v2
	v_sub_f32_e32 v2, v37, v51
	v_add_f32_e32 v10, v30, v10
	v_mul_f32_e32 v2, 0x3fb8aa3b, v2
	v_sub_f32_e32 v3, v49, v51
	v_add_f32_e32 v10, v31, v10
	v_exp_f32_e32 v2, v2
	v_mul_f32_e32 v3, 0x3fb8aa3b, v3
	v_sub_f32_e32 v4, v50, v51
	v_add_f32_e32 v10, v6, v10
	v_exp_f32_e32 v3, v3
	v_mul_f32_e32 v4, 0x3fb8aa3b, v4
	v_sub_f32_e32 v5, v52, v51
	v_add_f32_e32 v10, v7, v10
	v_exp_f32_e32 v4, v4
	v_mul_f32_e32 v5, 0x3fb8aa3b, v5
	v_add_f32_e32 v10, v8, v10
	v_exp_f32_e32 v5, v5
	v_add_f32_e32 v10, v9, v10
	v_add_f32_e32 v10, v2, v10
	v_lshrrev_b32_e32 v11, 2, v38
	v_lshrrev_b32_e32 v15, 2, v17
	v_add_f32_e32 v10, v3, v10
	v_and_b32_e32 v11, 60, v11
	v_and_b32_e32 v14, 15, v38
	v_and_b32_e32 v15, 60, v15
	v_and_b32_e32 v17, 15, v17
	v_lshrrev_b32_e32 v22, 2, v39
	v_and_b32_e32 v23, 15, v39
	v_and_b32_e32 v33, 15, v40
	v_add_f32_e32 v10, v4, v10
	v_add_u32_e32 v11, v16, v11
	v_lshl_add_u32 v14, v14, 2, v16
	v_add_u32_e32 v15, v16, v15
	v_lshl_add_u32 v17, v17, 2, v16
	v_and_b32_e32 v22, 60, v22
	v_lshl_add_u32 v23, v23, 2, v16
	v_and_b32_e32 v32, 60, v32
	v_lshl_add_u32 v33, v33, 2, v16
	v_add_f32_e32 v10, v5, v10
	v_add_u32_e32 v22, v16, v22
	v_add_u32_e32 v32, v16, v32
	ds_read_b32 v11, v11
	ds_read_b32 v14, v14 offset:64
	ds_read_b32 v15, v15
	ds_read_b32 v17, v17 offset:64
	ds_read_b32 v34, v22
	ds_read_b32 v23, v23 offset:64
	ds_read_b32 v35, v32
	ds_read_b32 v33, v33 offset:64
	s_waitcnt lgkmcnt(6)
	v_lshl_add_u32 v14, v11, 7, v14
	v_div_scale_f32 v11, s[4:5], v10, v10, 1.0
	v_rcp_f32_e32 v36, v11
	s_waitcnt lgkmcnt(4)
	v_lshl_add_u32 v22, v15, 7, v17
	s_waitcnt lgkmcnt(2)
	v_lshl_add_u32 v32, v34, 7, v23
	s_waitcnt lgkmcnt(0)
	v_lshl_add_u32 v34, v35, 7, v33
	v_fma_f32 v15, -v11, v36, 1.0
	v_fmac_f32_e32 v36, v15, v36
	v_div_scale_f32 v15, vcc, 1.0, v10, 1.0
	v_mul_f32_e32 v17, v15, v36
	v_fma_f32 v23, -v11, v17, v15
	v_fmac_f32_e32 v17, v23, v36
	v_fma_f32 v11, -v11, v17, v15
	v_div_fmas_f32 v11, v11, v36, v17
	v_div_fixup_f32 v10, v11, v10, 1.0
	v_pk_mul_f32 v[24:25], v[24:25], v[10:11] op_sel_hi:[1,0]
	v_pk_mul_f32 v[26:27], v[26:27], v[10:11] op_sel_hi:[1,0]
	v_ashrrev_i32_e32 v15, 31, v14
	v_ashrrev_i32_e32 v33, 31, v32
	v_lshl_add_u64 v[12:13], s[10:11], 0, v[12:13]
	v_ashrrev_i32_e32 v23, 31, v22
	v_lshlrev_b64 v[36:37], 2, v[32:33]
	v_lshl_add_u64 v[38:39], s[8:9], 0, v[36:37]
	v_ashrrev_i32_e32 v35, 31, v34
	s_waitcnt vmcnt(1)
	v_pk_mul_f32 v[18:19], v[24:25], v[194:195]
	v_lshlrev_b64 v[24:25], 2, v[14:15]
	v_pk_mul_f32 v[20:21], v[26:27], v[196:197]
	global_store_dwordx4 v[12:13], v[18:21], off
	v_lshlrev_b64 v[26:27], 2, v[22:23]
	s_nop 0
	v_lshl_add_u64 v[18:19], s[8:9], 0, v[24:25]
	v_lshl_add_u64 v[20:21], s[8:9], 0, v[26:27]
	v_lshlrev_b64 v[38:39], 2, v[34:35]
	v_lshl_add_u64 v[18:19], s[8:9], 0, v[38:39]
	v_lshrrev_b32_e32 v11, 9, v170
	v_and_or_b32 v18, v11, s3, v14
	v_lshrrev_b32_e32 v11, 9, v171
	v_and_or_b32 v19, v11, s3, v22
	v_lshrrev_b32_e32 v11, 9, v172
	v_and_or_b32 v20, v11, s3, v32
	v_lshrrev_b32_e32 v11, 9, v173
	v_and_or_b32 v21, v11, s3, v34
	global_store_dwordx4 v[0:1], v[18:21], off offset:16
	v_lshrrev_b32_e32 v11, 2, v41
	v_lshrrev_b32_e32 v15, 2, v42
	v_lshrrev_b32_e32 v18, 2, v43
	v_lshrrev_b32_e32 v20, 2, v44
	v_and_b32_e32 v11, 60, v11
	v_and_b32_e32 v14, 15, v41
	v_and_b32_e32 v15, 60, v15
	v_and_b32_e32 v17, 15, v42
	v_and_b32_e32 v18, 60, v18
	v_and_b32_e32 v19, 15, v43
	v_and_b32_e32 v20, 60, v20
	v_and_b32_e32 v21, 15, v44
	v_add_u32_e32 v11, v16, v11
	v_lshl_add_u32 v14, v14, 2, v16
	v_add_u32_e32 v15, v16, v15
	v_lshl_add_u32 v17, v17, 2, v16
	v_add_u32_e32 v18, v16, v18
	v_lshl_add_u32 v19, v19, 2, v16
	v_add_u32_e32 v20, v16, v20
	v_lshl_add_u32 v21, v21, 2, v16
	ds_read_b32 v11, v11
	ds_read_b32 v14, v14 offset:64
	ds_read_b32 v15, v15
	ds_read_b32 v17, v17 offset:64
	ds_read_b32 v18, v18
	ds_read_b32 v19, v19 offset:64
	ds_read_b32 v20, v20
	ds_read_b32 v21, v21 offset:64
	s_waitcnt lgkmcnt(6)
; #define RT_PK(q_) (ex[q_] | (int)((__float_as_uint(usc[ex[q_]]) >> 23) << 14))
;     __device__ __forceinline__ void fused(f32x4 (&acc)[2][2][4][2], const Unit& u, int wr, int wc, int fr, int fq, PG8_LAS unsigned char* lds, int wid, int lane) const {
;     ...
;             for (int q = 0; q < 16; ++q) { const unsigned cid = __float_as_uint(best[q]) & 255u; ex[q] = idxl[cid >> 4] * 128 + idxl[16 + (cid & 15u)]; }
;             const size_t o = ((size_t)u.pn * 16384 + (size_t)(u.pm * BM + row)) * 16;
;             typedef int i32x4 __attribute__((ext_vector_type(4)));
; #pragma unroll
;             for (int i = 0; i < 4; ++i) {
;     ...
;                 *(i32x4*)(eidx + o + 4 * i) = (i32x4){RT_PK(4 * i), RT_PK(4 * i + 1), RT_PK(4 * i + 2), RT_PK(4 * i + 3)};
;                 *(f32x4*)(egate + o + 4 * i) = (f32x4){sc[4 * i] * rs * vsc[ex[4 * i]], sc[4 * i + 1] * rs * vsc[ex[4 * i + 1]], sc[4 * i + 2] * rs * vsc[ex[4 * i + 2]], sc[4 * i + 3] * rs * vsc[ex[4 * i + 3]]};
	v_lshl_add_u32 v14, v11, 7, v14
	s_waitcnt lgkmcnt(4)
	v_lshl_add_u32 v22, v15, 7, v17
	s_waitcnt lgkmcnt(2)
	v_lshl_add_u32 v32, v18, 7, v19
	v_pk_mul_f32 v[18:19], v[28:29], v[10:11] op_sel_hi:[1,0]
	s_waitcnt lgkmcnt(0)
	v_lshl_add_u32 v34, v20, 7, v21
	v_pk_mul_f32 v[20:21], v[30:31], v[10:11] op_sel_hi:[1,0]
	v_ashrrev_i32_e32 v15, 31, v14
	v_ashrrev_i32_e32 v33, 31, v32
	v_ashrrev_i32_e32 v23, 31, v22
	v_lshlrev_b64 v[28:29], 2, v[32:33]
	v_lshl_add_u64 v[30:31], s[8:9], 0, v[28:29]
	v_ashrrev_i32_e32 v35, 31, v34
	v_pk_mul_f32 v[20:21], v[20:21], v[184:185]
	v_pk_mul_f32 v[18:19], v[18:19], v[182:183]
	v_lshlrev_b64 v[24:25], 2, v[14:15]
	global_store_dwordx4 v[12:13], v[18:21], off offset:16
	v_lshlrev_b64 v[26:27], 2, v[22:23]
	s_nop 0
	v_lshl_add_u64 v[18:19], s[8:9], 0, v[24:25]
	v_lshl_add_u64 v[20:21], s[8:9], 0, v[26:27]
	v_lshlrev_b64 v[30:31], 2, v[34:35]
	v_lshl_add_u64 v[18:19], s[8:9], 0, v[30:31]
	v_lshrrev_b32_e32 v11, 9, v174
	v_and_or_b32 v18, v11, s3, v14
	v_lshrrev_b32_e32 v11, 9, v175
	v_and_or_b32 v19, v11, s3, v22
	v_lshrrev_b32_e32 v11, 9, v176
	v_and_or_b32 v20, v11, s3, v32
	v_lshrrev_b32_e32 v11, 9, v177
	v_and_or_b32 v21, v11, s3, v34
	global_store_dwordx4 v[0:1], v[18:21], off offset:32
	v_lshrrev_b32_e32 v11, 2, v45
	v_lshrrev_b32_e32 v15, 2, v46
	v_lshrrev_b32_e32 v18, 2, v47
	v_lshrrev_b32_e32 v20, 2, v48
	v_and_b32_e32 v11, 60, v11
	v_and_b32_e32 v14, 15, v45
	v_and_b32_e32 v15, 60, v15
	v_and_b32_e32 v17, 15, v46
	v_and_b32_e32 v18, 60, v18
	v_and_b32_e32 v19, 15, v47
	v_and_b32_e32 v20, 60, v20
	v_add_u32_e32 v11, v16, v11
	v_lshl_add_u32 v14, v14, 2, v16
	v_add_u32_e32 v15, v16, v15
	v_lshl_add_u32 v17, v17, 2, v16
	v_add_u32_e32 v18, v16, v18
	v_lshl_add_u32 v19, v19, 2, v16
	v_add_u32_e32 v20, v16, v20
	v_and_b32_e32 v21, 15, v48
	v_lshl_add_u32 v16, v21, 2, v16
	ds_read_b32 v11, v11
	ds_read_b32 v14, v14 offset:64
	ds_read_b32 v15, v15
	ds_read_b32 v17, v17 offset:64
	ds_read_b32 v18, v18
	ds_read_b32 v19, v19 offset:64
	ds_read_b32 v20, v20
	ds_read_b32 v21, v16 offset:64
	s_waitcnt lgkmcnt(6)
	v_lshl_add_u32 v14, v11, 7, v14
	s_waitcnt lgkmcnt(4)
	v_lshl_add_u32 v16, v15, 7, v17
	s_waitcnt lgkmcnt(2)
	v_lshl_add_u32 v18, v18, 7, v19
	v_pk_mul_f32 v[6:7], v[6:7], v[10:11] op_sel_hi:[1,0]
	v_pk_mul_f32 v[8:9], v[8:9], v[10:11] op_sel_hi:[1,0]
	v_ashrrev_i32_e32 v15, 31, v14
	v_ashrrev_i32_e32 v19, 31, v18
	s_waitcnt lgkmcnt(0)
	v_lshl_add_u32 v20, v20, 7, v21
	v_lshlrev_b64 v[22:23], 2, v[14:15]
	v_ashrrev_i32_e32 v17, 31, v16
	v_ashrrev_i32_e32 v21, 31, v20
	v_pk_mul_f32 v[8:9], v[8:9], v[188:189]
	v_pk_mul_f32 v[6:7], v[6:7], v[186:187]
	v_lshlrev_b64 v[26:27], 2, v[18:19]
	global_store_dwordx4 v[12:13], v[6:9], off offset:32
	v_lshlrev_b64 v[24:25], 2, v[16:17]
	v_lshl_add_u64 v[28:29], s[8:9], 0, v[26:27]
	v_lshl_add_u64 v[6:7], s[8:9], 0, v[22:23]
	v_lshl_add_u64 v[8:9], s[8:9], 0, v[24:25]
	v_lshlrev_b64 v[28:29], 2, v[20:21]
	v_lshl_add_u64 v[6:7], s[8:9], 0, v[28:29]
	v_lshrrev_b32_e32 v6, 9, v178
	v_lshrrev_b32_e32 v7, 9, v179
	v_lshrrev_b32_e32 v8, 9, v180
	v_and_or_b32 v6, v6, s3, v14
	v_and_or_b32 v7, v7, s3, v16
	v_lshrrev_b32_e32 v9, 9, v181
	v_and_or_b32 v8, v8, s3, v18
	v_and_or_b32 v9, v9, s3, v20
	global_store_dwordx4 v[0:1], v[6:9], off offset:48
	v_pk_mul_f32 v[0:1], v[2:3], v[10:11] op_sel_hi:[1,0]
	v_pk_mul_f32 v[2:3], v[4:5], v[10:11] op_sel_hi:[1,0]
	v_pk_mul_f32 v[0:1], v[0:1], v[190:191]
	v_pk_mul_f32 v[2:3], v[2:3], v[192:193]
	global_store_dwordx4 v[12:13], v[0:3], off offset:48
